# speedup vs baseline: 1.0337x; 1.0067x over previous
_Z5gemm8ILi128ELi2ELi4ELi4ELi2ELi32EEvPKDF16_S1_iiiPDF16_PfPKf:
	s_load_dwordx8 s[4:11], s[0:1], 0x0
	s_lshl_b32 s3, s2, 2
	s_waitcnt lgkmcnt(0)
	s_and_b32 s11, s2, 4
	s_lshr_b32 s12, s2, 6
	s_bfe_u32 s13, s2, 0x30003
	s_add_i32 s11, s11, s12
	s_and_b32 s12, s2, 1
	s_and_b32 s2, s3, 8
	s_or_b32 s2, s2, s13
	s_lshl_b32 s13, s2, 7
	s_lshr_b32 s2, s10, 31
	s_add_i32 s2, s10, s2
	s_ashr_i32 s14, s2, 1
	s_mul_hi_i32 s3, s10, s13
	s_mul_i32 s2, s10, s13
	s_lshl_b32 s11, s11, 7
	s_lshl_b64 s[2:3], s[2:3], 1
	v_lshrrev_b32_e32 v2, 4, v0
	s_add_u32 s15, s4, s2
	s_mul_i32 s2, s14, s12
	v_xor_b32_e32 v1, v2, v0
	v_or_b32_e32 v4, 0x200, v0
	s_addc_u32 s16, s5, s3
	s_ashr_i32 s3, s2, 31
	v_lshlrev_b32_e32 v1, 3, v1
	v_lshrrev_b32_e32 v3, 3, v0
	v_lshrrev_b32_e32 v4, 3, v4
	s_lshl_b64 s[4:5], s[2:3], 1
	v_and_b32_e32 v1, 56, v1
	v_mul_lo_u32 v3, v3, s10
	v_mul_lo_u32 v4, v4, s10
	s_add_u32 s2, s15, s4
	s_mul_hi_i32 s15, s10, s11
	s_mul_i32 s14, s10, s11
	v_lshlrev_b32_e32 v106, 4, v0
	v_add_lshl_u32 v3, v3, v1, 1
	v_add_lshl_u32 v4, v4, v1, 1
	s_addc_u32 s3, s16, s5
	s_lshl_b64 s[14:15], s[14:15], 1
	v_add_u32_e32 v1, 0, v106
	s_add_u32 s6, s6, s14
	v_readfirstlane_b32 s18, v1
	v_add_u32_e32 v5, 0x2000, v1
	s_addc_u32 s7, s7, s15
	s_mov_b32 m0, s18
	v_readfirstlane_b32 s15, v5
	v_add_u32_e32 v5, 0x4000, v1
	s_add_u32 s4, s6, s4
	global_load_lds_dwordx4 v3, s[2:3]
	s_mov_b32 m0, s15
	v_readfirstlane_b32 s16, v5
	v_add_u32_e32 v5, 0x6000, v1
	s_addc_u32 s5, s7, s5
	global_load_lds_dwordx4 v4, s[2:3]
	s_mov_b32 m0, s16
	v_readfirstlane_b32 s17, v5
	v_add_u32_e32 v5, 0x8000, v1
	global_load_lds_dwordx4 v3, s[4:5]
	s_mov_b32 m0, s17
	s_add_u32 s20, s2, 0x80
	v_readfirstlane_b32 s14, v5
	v_add_u32_e32 v5, 0xa000, v1
	global_load_lds_dwordx4 v4, s[4:5]
	s_addc_u32 s21, s3, 0
	s_mov_b32 m0, s14
	v_readfirstlane_b32 s6, v5
	v_add_u32_e32 v5, 0xc000, v1
	s_add_u32 s22, s4, 0x80
	global_load_lds_dwordx4 v3, s[20:21]
	s_mov_b32 m0, s6
	v_readfirstlane_b32 s7, v5
	v_add_u32_e32 v5, 0xe000, v1
	s_addc_u32 s23, s5, 0
	global_load_lds_dwordx4 v4, s[20:21]
	s_mov_b32 m0, s7
	v_readfirstlane_b32 s10, v5
	v_add_u32_e32 v5, 0x10000, v1
	global_load_lds_dwordx4 v3, s[22:23]
	s_mov_b32 m0, s10
	s_add_u32 s20, s2, 0x100
	v_readfirstlane_b32 s19, v5
	v_add_u32_e32 v5, 0x12000, v1
	global_load_lds_dwordx4 v4, s[22:23]
	s_addc_u32 s21, s3, 0
	s_mov_b32 m0, s19
	v_readfirstlane_b32 s19, v5
	v_add_u32_e32 v5, 0x14000, v1
	s_add_u32 s22, s4, 0x100
	global_load_lds_dwordx4 v3, s[20:21]
	s_mov_b32 m0, s19
	v_readfirstlane_b32 s19, v5
	v_add_u32_e32 v5, 0x16000, v1
	s_addc_u32 s23, s5, 0
	global_load_lds_dwordx4 v4, s[20:21]
	s_mov_b32 m0, s19
	v_readfirstlane_b32 s19, v5
	v_add_u32_e32 v5, 0x18000, v1
	global_load_lds_dwordx4 v3, s[22:23]
	s_mov_b32 m0, s19
	s_add_u32 s20, s2, 0x180
	v_readfirstlane_b32 s19, v5
	v_add_u32_e32 v5, 0x1a000, v1
	global_load_lds_dwordx4 v4, s[22:23]
	s_addc_u32 s21, s3, 0
	s_mov_b32 m0, s19
	v_readfirstlane_b32 s19, v5
	v_add_u32_e32 v5, 0x1c000, v1
	s_add_u32 s22, s4, 0x180
	global_load_lds_dwordx4 v3, s[20:21]
	s_mov_b32 m0, s19
	v_readfirstlane_b32 s19, v5
	v_add_u32_e32 v1, 0x1e000, v1
	s_addc_u32 s23, s5, 0
	global_load_lds_dwordx4 v4, s[20:21]
	s_mov_b32 m0, s19
	v_readfirstlane_b32 s19, v1
	global_load_lds_dwordx4 v3, s[22:23]
	s_mov_b32 m0, s19
	v_bfe_u32 v8, v0, 1, 3
	global_load_lds_dwordx4 v4, s[22:23]
	v_lshrrev_b32_e32 v6, 1, v0
	v_bitop3_b32 v2, v2, v8, 3 bitop3:0x6c
	v_and_b32_e32 v5, 15, v0
	v_lshrrev_b32_e32 v1, 2, v0
	v_lshlrev_b32_e32 v7, 4, v2
	v_and_b32_e32 v2, 0x60, v6
	v_and_or_b32 v1, v1, 64, v5
	v_or_b32_e32 v5, v2, v5
	v_lshlrev_b32_e32 v6, 7, v5
	v_lshlrev_b32_e32 v102, 7, v1
	v_add_u32_e32 v9, 0, v6
	v_add_u32_e32 v38, 0, v102
	s_waitcnt vmcnt(12)
	s_barrier
	v_add_u32_e32 v5, v9, v7
	v_add_u32_e32 v7, v38, v7
	ds_read_b128 v[10:13], v5 offset:18432
	ds_read_b128 v[14:17], v5 offset:16384
	ds_read_b128 v[18:21], v7
	ds_read_b128 v[22:25], v7 offset:2048
	ds_read_b128 v[30:33], v7 offset:4096
	ds_read_b128 v[34:37], v7 offset:6144
	s_load_dwordx2 s[0:1], s[0:1], 0x20
	v_bfe_u32 v0, v0, 4, 2
	v_bitop3_b32 v8, v0, v8, 4 bitop3:0x36
	v_or_b32_e32 v103, 0x4000, v6
	s_waitcnt lgkmcnt(0)
	v_mfma_f32_16x16x32_f16 v[26:29], v[14:17], v[18:21], 0
	v_lshlrev_b32_e32 v104, 4, v8
	v_mfma_f32_16x16x32_f16 v[18:21], v[10:13], v[18:21], 0
	v_add_u32_e32 v6, v38, v104
	ds_read_b128 v[38:41], v6
	ds_read_b128 v[42:45], v6 offset:2048
	ds_read_b128 v[46:49], v6 offset:4096
	ds_read_b128 v[50:53], v6 offset:6144
	v_add_u32_e32 v8, v9, v104
	ds_read_b128 v[54:57], v8 offset:16384
	ds_read_b128 v[58:61], v8 offset:18432
	v_mfma_f32_16x16x32_f16 v[62:65], v[14:17], v[22:25], 0
	v_mfma_f32_16x16x32_f16 v[22:25], v[10:13], v[22:25], 0
	v_mfma_f32_16x16x32_f16 v[66:69], v[14:17], v[30:33], 0
	v_mfma_f32_16x16x32_f16 v[30:33], v[10:13], v[30:33], 0
	v_mfma_f32_16x16x32_f16 v[14:17], v[14:17], v[34:37], 0
	v_mfma_f32_16x16x32_f16 v[10:13], v[10:13], v[34:37], 0
	s_add_u32 s20, s2, 0x200
	s_mov_b32 m0, s18
	s_waitcnt vmcnt(8) lgkmcnt(0)
	s_barrier
	s_addc_u32 s21, s3, 0
	s_add_u32 s22, s4, 0x200
	global_load_lds_dwordx4 v3, s[20:21]
	s_mov_b32 m0, s15
	s_addc_u32 s23, s5, 0
	global_load_lds_dwordx4 v4, s[20:21]
	s_mov_b32 m0, s16
	s_nop 0
	global_load_lds_dwordx4 v3, s[22:23]
	s_mov_b32 m0, s17
	s_nop 0
	global_load_lds_dwordx4 v4, s[22:23]
	s_waitcnt lgkmcnt(0)
	v_mfma_f32_16x16x32_f16 v[26:29], v[54:57], v[38:41], v[26:29]
	v_mfma_f32_16x16x32_f16 v[18:21], v[58:61], v[38:41], v[18:21]
	ds_read_b128 v[34:37], v7 offset:32768
	ds_read_b128 v[38:41], v7 offset:34816
	ds_read_b128 v[70:73], v7 offset:36864
	ds_read_b128 v[74:77], v7 offset:38912
	ds_read_b128 v[78:81], v5 offset:49152
	ds_read_b128 v[82:85], v5 offset:51200
	v_mfma_f32_16x16x32_f16 v[62:65], v[54:57], v[42:45], v[62:65]
	v_mfma_f32_16x16x32_f16 v[22:25], v[58:61], v[42:45], v[22:25]
	v_mfma_f32_16x16x32_f16 v[42:45], v[54:57], v[46:49], v[66:69]
	v_mfma_f32_16x16x32_f16 v[30:33], v[58:61], v[46:49], v[30:33]
	v_mfma_f32_16x16x32_f16 v[14:17], v[54:57], v[50:53], v[14:17]
	v_mfma_f32_16x16x32_f16 v[10:13], v[58:61], v[50:53], v[10:13]
	s_waitcnt lgkmcnt(0)
	v_mfma_f32_16x16x32_f16 v[26:29], v[78:81], v[34:37], v[26:29]
	v_mfma_f32_16x16x32_f16 v[18:21], v[82:85], v[34:37], v[18:21]
	ds_read_b128 v[34:37], v6 offset:32768
	ds_read_b128 v[46:49], v6 offset:34816
	ds_read_b128 v[50:53], v6 offset:36864
	ds_read_b128 v[54:57], v6 offset:38912
	ds_read_b128 v[58:61], v8 offset:49152
	ds_read_b128 v[66:69], v8 offset:51200
	v_mfma_f32_16x16x32_f16 v[62:65], v[78:81], v[38:41], v[62:65]
	v_mfma_f32_16x16x32_f16 v[22:25], v[82:85], v[38:41], v[22:25]
	v_mfma_f32_16x16x32_f16 v[38:41], v[78:81], v[70:73], v[42:45]
	v_mfma_f32_16x16x32_f16 v[30:33], v[82:85], v[70:73], v[30:33]
	v_mfma_f32_16x16x32_f16 v[42:45], v[78:81], v[74:77], v[14:17]
	v_mfma_f32_16x16x32_f16 v[70:73], v[82:85], v[74:77], v[10:13]
	s_add_u32 s20, s2, 0x280
	s_mov_b32 m0, s14
	s_waitcnt vmcnt(8) lgkmcnt(0)
	s_barrier
	s_addc_u32 s21, s3, 0
	s_add_u32 s22, s4, 0x280
	global_load_lds_dwordx4 v3, s[20:21]
	s_mov_b32 m0, s6
	s_addc_u32 s23, s5, 0
	global_load_lds_dwordx4 v4, s[20:21]
	s_mov_b32 m0, s7
	s_nop 0
	global_load_lds_dwordx4 v3, s[22:23]
	s_mov_b32 m0, s10
	s_nop 0
	global_load_lds_dwordx4 v4, s[22:23]
	s_waitcnt lgkmcnt(0)
	v_mfma_f32_16x16x32_f16 v[26:29], v[58:61], v[34:37], v[26:29]
	v_mfma_f32_16x16x32_f16 v[16:19], v[66:69], v[34:37], v[18:21]
	v_add_u32_e32 v9, 0x10000, v7
	v_add_u32_e32 v11, 0x11000, v7
	v_add_u32_e32 v13, 0x14000, v5
	v_add_u32_e32 v10, 0x10800, v7
	ds_read_b128 v[34:37], v9
	ds_read_b128 v[74:77], v10
	v_add_u32_e32 v12, 0x11800, v7
	ds_read_b128 v[78:81], v11
	ds_read_b128 v[82:85], v12
	v_add_u32_e32 v14, 0x14800, v5
	ds_read_b128 v[86:89], v13
	ds_read_b128 v[90:93], v14
	v_mfma_f32_16x16x32_f16 v[62:65], v[58:61], v[46:49], v[62:65]
	v_mfma_f32_16x16x32_f16 v[20:23], v[66:69], v[46:49], v[22:25]
	v_mfma_f32_16x16x32_f16 v[38:41], v[58:61], v[50:53], v[38:41]
	v_mfma_f32_16x16x32_f16 v[30:33], v[66:69], v[50:53], v[30:33]
	v_mfma_f32_16x16x32_f16 v[42:45], v[58:61], v[54:57], v[42:45]
	v_mfma_f32_16x16x32_f16 v[46:49], v[66:69], v[54:57], v[70:73]
	s_waitcnt lgkmcnt(0)
	v_mfma_f32_16x16x32_f16 v[24:27], v[86:89], v[34:37], v[26:29]
	v_mfma_f32_16x16x32_f16 v[34:37], v[90:93], v[34:37], v[16:19]
	s_add_i32 s19, 0, 0x10000
	s_nop 1
	v_add_u32_e32 v16, s19, v104
	v_add_u32_e32 v15, v16, v102
	ds_read_b128 v[50:53], v15
	ds_read_b128 v[54:57], v15 offset:2048
	ds_read_b128 v[58:61], v15 offset:4096
	ds_read_b128 v[66:69], v15 offset:6144
	v_add_u32_e32 v16, v16, v103
	ds_read_b128 v[70:73], v16
	ds_read_b128 v[94:97], v16 offset:2048
	v_mfma_f32_16x16x32_f16 v[62:65], v[86:89], v[74:77], v[62:65]
	v_mfma_f32_16x16x32_f16 v[74:77], v[90:93], v[74:77], v[20:23]
	v_mfma_f32_16x16x32_f16 v[38:41], v[86:89], v[78:81], v[38:41]
	v_mfma_f32_16x16x32_f16 v[28:31], v[90:93], v[78:81], v[30:33]
	v_mfma_f32_16x16x32_f16 v[42:45], v[86:89], v[82:85], v[42:45]
	v_mfma_f32_16x16x32_f16 v[46:49], v[90:93], v[82:85], v[46:49]
	v_add_u32_e32 v17, s19, v106
	s_add_u32 s20, s2, 0x300
	v_readfirstlane_b32 s22, v17
	v_add_u32_e32 v18, 0x2000, v17
	s_waitcnt vmcnt(8) lgkmcnt(0)
	s_barrier
	s_addc_u32 s21, s3, 0
	s_mov_b32 m0, s22
	v_readfirstlane_b32 s19, v18
	global_load_lds_dwordx4 v3, s[20:21]
	s_mov_b32 m0, s19
	v_add_u32_e32 v18, 0x4000, v17
	s_add_u32 s24, s4, 0x300
	global_load_lds_dwordx4 v4, s[20:21]
	v_readfirstlane_b32 s20, v18
	v_add_u32_e32 v17, 0x6000, v17
	s_addc_u32 s25, s5, 0
	s_mov_b32 m0, s20
	v_readfirstlane_b32 s21, v17
	global_load_lds_dwordx4 v3, s[24:25]
	s_mov_b32 m0, s21
	s_nop 0
	global_load_lds_dwordx4 v4, s[24:25]
	s_waitcnt lgkmcnt(0)
	v_mfma_f32_16x16x32_f16 v[24:27], v[70:73], v[50:53], v[24:27]
	v_mfma_f32_16x16x32_f16 v[32:35], v[94:97], v[50:53], v[34:37]
	v_add_u32_e32 v17, 0x18000, v7
	v_add_u32_e32 v19, 0x19000, v7
	v_add_u32_e32 v21, 0x1c000, v5
	v_add_u32_e32 v18, 0x18800, v7
	ds_read_b128 v[50:53], v17
	ds_read_b128 v[78:81], v18
	v_add_u32_e32 v20, 0x19800, v7
	ds_read_b128 v[82:85], v19
	ds_read_b128 v[86:89], v20
	v_add_u32_e32 v22, 0x1c800, v5
	ds_read_b128 v[90:93], v21
	ds_read_b128 v[98:101], v22
	v_mfma_f32_16x16x32_f16 v[62:65], v[70:73], v[54:57], v[62:65]
	v_mfma_f32_16x16x32_f16 v[54:57], v[94:97], v[54:57], v[74:77]
	v_mfma_f32_16x16x32_f16 v[36:39], v[70:73], v[58:61], v[38:41]
	v_mfma_f32_16x16x32_f16 v[28:31], v[94:97], v[58:61], v[28:31]
	v_mfma_f32_16x16x32_f16 v[40:43], v[70:73], v[66:69], v[42:45]
	v_mfma_f32_16x16x32_f16 v[44:47], v[94:97], v[66:69], v[46:49]
	s_waitcnt lgkmcnt(0)
	v_mfma_f32_16x16x32_f16 v[58:61], v[90:93], v[50:53], v[24:27]
	v_mfma_f32_16x16x32_f16 v[32:35], v[98:101], v[50:53], v[32:35]
	s_add_i32 s23, 0, 0x18000
	s_nop 0
	v_add_u32_e32 v24, s23, v104
	v_add_u32_e32 v23, v24, v102
	ds_read_b128 v[48:51], v23
	ds_read_b128 v[66:69], v23 offset:2048
	ds_read_b128 v[70:73], v23 offset:4096
	ds_read_b128 v[74:77], v23 offset:6144
	v_add_u32_e32 v24, v24, v103
	ds_read_b128 v[94:97], v24
	ds_read_b128 v[102:105], v24 offset:2048
	v_mfma_f32_16x16x32_f16 v[62:65], v[90:93], v[78:81], v[62:65]
	v_mfma_f32_16x16x32_f16 v[52:55], v[98:101], v[78:81], v[54:57]
	v_mfma_f32_16x16x32_f16 v[36:39], v[90:93], v[82:85], v[36:39]
	v_mfma_f32_16x16x32_f16 v[26:29], v[98:101], v[82:85], v[28:31]
	v_mfma_f32_16x16x32_f16 v[40:43], v[90:93], v[86:89], v[40:43]
	v_mfma_f32_16x16x32_f16 v[44:47], v[98:101], v[86:89], v[44:47]
	v_add_u32_e32 v25, s23, v106
	s_add_u32 s24, s2, 0x380
	v_readfirstlane_b32 s26, v25
	v_add_u32_e32 v30, 0x2000, v25
	s_waitcnt vmcnt(8) lgkmcnt(0)
	s_barrier
	s_addc_u32 s25, s3, 0
	s_mov_b32 m0, s26
	v_readfirstlane_b32 s23, v30
	global_load_lds_dwordx4 v3, s[24:25]
	s_mov_b32 m0, s23
	v_add_u32_e32 v30, 0x4000, v25
	s_add_u32 s28, s4, 0x380
	global_load_lds_dwordx4 v4, s[24:25]
	v_readfirstlane_b32 s24, v30
	v_add_u32_e32 v25, 0x6000, v25
	s_addc_u32 s29, s5, 0
	s_mov_b32 m0, s24
	v_readfirstlane_b32 s25, v25
	global_load_lds_dwordx4 v3, s[28:29]
	s_mov_b32 m0, s25
	s_nop 0
	global_load_lds_dwordx4 v4, s[28:29]
	s_waitcnt lgkmcnt(0)
	v_mfma_f32_16x16x32_f16 v[56:59], v[94:97], v[48:51], v[58:61]
	v_mfma_f32_16x16x32_f16 v[30:33], v[102:105], v[48:51], v[32:35]
	ds_read_b128 v[48:51], v7
	ds_read_b128 v[78:81], v7 offset:2048
	ds_read_b128 v[82:85], v7 offset:4096
	ds_read_b128 v[86:89], v7 offset:6144
	ds_read_b128 v[90:93], v5 offset:16384
	ds_read_b128 v[98:101], v5 offset:18432
	v_mfma_f32_16x16x32_f16 v[60:63], v[94:97], v[66:69], v[62:65]
	v_mfma_f32_16x16x32_f16 v[52:55], v[102:105], v[66:69], v[52:55]
	v_mfma_f32_16x16x32_f16 v[34:37], v[94:97], v[70:73], v[36:39]
	v_mfma_f32_16x16x32_f16 v[26:29], v[102:105], v[70:73], v[26:29]
	v_mfma_f32_16x16x32_f16 v[38:41], v[94:97], v[74:77], v[40:43]
	v_mfma_f32_16x16x32_f16 v[42:45], v[102:105], v[74:77], v[44:47]
	s_waitcnt lgkmcnt(0)
	v_mfma_f32_16x16x32_f16 v[56:59], v[90:93], v[48:51], v[56:59]
	v_mfma_f32_16x16x32_f16 v[30:33], v[98:101], v[48:51], v[30:33]
	ds_read_b128 v[46:49], v6
	ds_read_b128 v[64:67], v6 offset:2048
	ds_read_b128 v[68:71], v6 offset:4096
	ds_read_b128 v[72:75], v6 offset:6144
	ds_read_b128 v[94:97], v8 offset:16384
	ds_read_b128 v[102:105], v8 offset:18432
	v_mfma_f32_16x16x32_f16 v[60:63], v[90:93], v[78:81], v[60:63]
	v_mfma_f32_16x16x32_f16 v[50:53], v[98:101], v[78:81], v[52:55]
	v_mfma_f32_16x16x32_f16 v[34:37], v[90:93], v[82:85], v[34:37]
	v_mfma_f32_16x16x32_f16 v[26:29], v[98:101], v[82:85], v[26:29]
	v_mfma_f32_16x16x32_f16 v[38:41], v[90:93], v[86:89], v[38:41]
	v_mfma_f32_16x16x32_f16 v[42:45], v[98:101], v[86:89], v[42:45]
	s_add_u32 s28, s2, 0x400
	s_mov_b32 m0, s18
	s_waitcnt vmcnt(8) lgkmcnt(0)
	s_barrier
	s_addc_u32 s29, s3, 0
	s_add_u32 s30, s4, 0x400
	global_load_lds_dwordx4 v3, s[28:29]
	s_mov_b32 m0, s15
	s_addc_u32 s31, s5, 0
	global_load_lds_dwordx4 v4, s[28:29]
	s_mov_b32 m0, s16
	s_nop 0
	global_load_lds_dwordx4 v3, s[30:31]
	s_mov_b32 m0, s17
	s_nop 0
	global_load_lds_dwordx4 v4, s[30:31]
	s_waitcnt lgkmcnt(0)
	v_mfma_f32_16x16x32_f16 v[54:57], v[94:97], v[46:49], v[56:59]
	v_mfma_f32_16x16x32_f16 v[30:33], v[102:105], v[46:49], v[30:33]
	ds_read_b128 v[46:49], v7 offset:32768
	ds_read_b128 v[76:79], v7 offset:34816
	ds_read_b128 v[80:83], v7 offset:36864
	ds_read_b128 v[84:87], v7 offset:38912
	ds_read_b128 v[88:91], v5 offset:49152
	ds_read_b128 v[98:101], v5 offset:51200
	v_mfma_f32_16x16x32_f16 v[58:61], v[94:97], v[64:67], v[60:63]
	v_mfma_f32_16x16x32_f16 v[50:53], v[102:105], v[64:67], v[50:53]
	v_mfma_f32_16x16x32_f16 v[34:37], v[94:97], v[68:71], v[34:37]
	v_mfma_f32_16x16x32_f16 v[26:29], v[102:105], v[68:71], v[26:29]
	v_mfma_f32_16x16x32_f16 v[38:41], v[94:97], v[72:75], v[38:41]
	v_mfma_f32_16x16x32_f16 v[42:45], v[102:105], v[72:75], v[42:45]
	s_waitcnt lgkmcnt(0)
	v_mfma_f32_16x16x32_f16 v[54:57], v[88:91], v[46:49], v[54:57]
	v_mfma_f32_16x16x32_f16 v[30:33], v[98:101], v[46:49], v[30:33]
	ds_read_b128 v[46:49], v6 offset:32768
	ds_read_b128 v[62:65], v6 offset:34816
	ds_read_b128 v[66:69], v6 offset:36864
	ds_read_b128 v[70:73], v6 offset:38912
	ds_read_b128 v[92:95], v8 offset:49152
	ds_read_b128 v[102:105], v8 offset:51200
	v_mfma_f32_16x16x32_f16 v[58:61], v[88:91], v[76:79], v[58:61]
	v_mfma_f32_16x16x32_f16 v[50:53], v[98:101], v[76:79], v[50:53]
	v_mfma_f32_16x16x32_f16 v[34:37], v[88:91], v[80:83], v[34:37]
	v_mfma_f32_16x16x32_f16 v[26:29], v[98:101], v[80:83], v[26:29]
	v_mfma_f32_16x16x32_f16 v[38:41], v[88:91], v[84:87], v[38:41]
	v_mfma_f32_16x16x32_f16 v[42:45], v[98:101], v[84:87], v[42:45]
	s_add_u32 s28, s2, 0x480
	s_mov_b32 m0, s14
	s_waitcnt vmcnt(8) lgkmcnt(0)
	s_barrier
	s_addc_u32 s29, s3, 0
	s_add_u32 s30, s4, 0x480
	global_load_lds_dwordx4 v3, s[28:29]
	s_mov_b32 m0, s6
	s_addc_u32 s31, s5, 0
	global_load_lds_dwordx4 v4, s[28:29]
	s_mov_b32 m0, s7
	s_nop 0
	global_load_lds_dwordx4 v3, s[30:31]
	s_mov_b32 m0, s10
	s_nop 0
	global_load_lds_dwordx4 v4, s[30:31]
	s_waitcnt lgkmcnt(0)
	v_mfma_f32_16x16x32_f16 v[54:57], v[92:95], v[46:49], v[54:57]
	v_mfma_f32_16x16x32_f16 v[30:33], v[102:105], v[46:49], v[30:33]
	ds_read_b128 v[46:49], v9
	ds_read_b128 v[74:77], v10
	ds_read_b128 v[78:81], v11
	ds_read_b128 v[82:85], v12
	ds_read_b128 v[86:89], v13
	ds_read_b128 v[96:99], v14
	v_mfma_f32_16x16x32_f16 v[58:61], v[92:95], v[62:65], v[58:61]
	v_mfma_f32_16x16x32_f16 v[50:53], v[102:105], v[62:65], v[50:53]
	v_mfma_f32_16x16x32_f16 v[34:37], v[92:95], v[66:69], v[34:37]
	v_mfma_f32_16x16x32_f16 v[26:29], v[102:105], v[66:69], v[26:29]
	v_mfma_f32_16x16x32_f16 v[38:41], v[92:95], v[70:73], v[38:41]
	v_mfma_f32_16x16x32_f16 v[42:45], v[102:105], v[70:73], v[42:45]
	s_waitcnt lgkmcnt(0)
	v_mfma_f32_16x16x32_f16 v[54:57], v[86:89], v[46:49], v[54:57]
	v_mfma_f32_16x16x32_f16 v[30:33], v[96:99], v[46:49], v[30:33]
	ds_read_b128 v[46:49], v15
	ds_read_b128 v[62:65], v15 offset:2048
	ds_read_b128 v[66:69], v15 offset:4096
	ds_read_b128 v[70:73], v15 offset:6144
	ds_read_b128 v[90:93], v16
	ds_read_b128 v[100:103], v16 offset:2048
	v_mfma_f32_16x16x32_f16 v[58:61], v[86:89], v[74:77], v[58:61]
	v_mfma_f32_16x16x32_f16 v[50:53], v[96:99], v[74:77], v[50:53]
	v_mfma_f32_16x16x32_f16 v[34:37], v[86:89], v[78:81], v[34:37]
	v_mfma_f32_16x16x32_f16 v[26:29], v[96:99], v[78:81], v[26:29]
	v_mfma_f32_16x16x32_f16 v[38:41], v[86:89], v[82:85], v[38:41]
	v_mfma_f32_16x16x32_f16 v[42:45], v[96:99], v[82:85], v[42:45]
	s_add_u32 s28, s2, 0x500
	s_mov_b32 m0, s22
	s_waitcnt vmcnt(8) lgkmcnt(0)
	s_barrier
	s_addc_u32 s29, s3, 0
	s_add_u32 s30, s4, 0x500
	global_load_lds_dwordx4 v3, s[28:29]
	s_mov_b32 m0, s19
	s_addc_u32 s31, s5, 0
	global_load_lds_dwordx4 v4, s[28:29]
	s_mov_b32 m0, s20
	s_nop 0
	global_load_lds_dwordx4 v3, s[30:31]
	s_mov_b32 m0, s21
	s_nop 0
	global_load_lds_dwordx4 v4, s[30:31]
	s_waitcnt lgkmcnt(0)
	v_mfma_f32_16x16x32_f16 v[54:57], v[90:93], v[46:49], v[54:57]
	v_mfma_f32_16x16x32_f16 v[30:33], v[100:103], v[46:49], v[30:33]
	ds_read_b128 v[46:49], v17
	ds_read_b128 v[74:77], v18
	ds_read_b128 v[78:81], v19
	ds_read_b128 v[82:85], v20
	ds_read_b128 v[86:89], v21
	ds_read_b128 v[94:97], v22
	v_mfma_f32_16x16x32_f16 v[58:61], v[90:93], v[62:65], v[58:61]
	v_mfma_f32_16x16x32_f16 v[50:53], v[100:103], v[62:65], v[50:53]
	v_mfma_f32_16x16x32_f16 v[34:37], v[90:93], v[66:69], v[34:37]
	v_mfma_f32_16x16x32_f16 v[26:29], v[100:103], v[66:69], v[26:29]
	v_mfma_f32_16x16x32_f16 v[38:41], v[90:93], v[70:73], v[38:41]
	v_mfma_f32_16x16x32_f16 v[42:45], v[100:103], v[70:73], v[42:45]
	s_waitcnt lgkmcnt(0)
	v_mfma_f32_16x16x32_f16 v[54:57], v[86:89], v[46:49], v[54:57]
	v_mfma_f32_16x16x32_f16 v[30:33], v[94:97], v[46:49], v[30:33]
	ds_read_b128 v[46:49], v23
	ds_read_b128 v[62:65], v23 offset:2048
	ds_read_b128 v[66:69], v23 offset:4096
	ds_read_b128 v[70:73], v23 offset:6144
	ds_read_b128 v[90:93], v24
	ds_read_b128 v[98:101], v24 offset:2048
	v_mfma_f32_16x16x32_f16 v[58:61], v[86:89], v[74:77], v[58:61]
	v_mfma_f32_16x16x32_f16 v[50:53], v[94:97], v[74:77], v[50:53]
	v_mfma_f32_16x16x32_f16 v[34:37], v[86:89], v[78:81], v[34:37]
	v_mfma_f32_16x16x32_f16 v[26:29], v[94:97], v[78:81], v[26:29]
	v_mfma_f32_16x16x32_f16 v[38:41], v[86:89], v[82:85], v[38:41]
	v_mfma_f32_16x16x32_f16 v[42:45], v[94:97], v[82:85], v[42:45]
	s_add_u32 s28, s2, 0x580
	s_mov_b32 m0, s26
	s_waitcnt vmcnt(8) lgkmcnt(0)
	s_barrier
	s_addc_u32 s29, s3, 0
	s_add_u32 s30, s4, 0x580
	global_load_lds_dwordx4 v3, s[28:29]
	s_mov_b32 m0, s23
	s_addc_u32 s31, s5, 0
	global_load_lds_dwordx4 v4, s[28:29]
	s_mov_b32 m0, s24
	s_nop 0
	global_load_lds_dwordx4 v3, s[30:31]
	s_mov_b32 m0, s25
	s_nop 0
	global_load_lds_dwordx4 v4, s[30:31]
	s_waitcnt lgkmcnt(0)
	v_mfma_f32_16x16x32_f16 v[54:57], v[90:93], v[46:49], v[54:57]
	v_mfma_f32_16x16x32_f16 v[30:33], v[98:101], v[46:49], v[30:33]
	ds_read_b128 v[46:49], v7
	ds_read_b128 v[74:77], v7 offset:2048
	ds_read_b128 v[78:81], v7 offset:4096
	ds_read_b128 v[82:85], v7 offset:6144
	ds_read_b128 v[86:89], v5 offset:16384
	ds_read_b128 v[94:97], v5 offset:18432
	v_mfma_f32_16x16x32_f16 v[58:61], v[90:93], v[62:65], v[58:61]
	v_mfma_f32_16x16x32_f16 v[50:53], v[98:101], v[62:65], v[50:53]
	v_mfma_f32_16x16x32_f16 v[34:37], v[90:93], v[66:69], v[34:37]
	v_mfma_f32_16x16x32_f16 v[26:29], v[98:101], v[66:69], v[26:29]
	v_mfma_f32_16x16x32_f16 v[38:41], v[90:93], v[70:73], v[38:41]
	v_mfma_f32_16x16x32_f16 v[42:45], v[98:101], v[70:73], v[42:45]
	s_waitcnt lgkmcnt(0)
	v_mfma_f32_16x16x32_f16 v[54:57], v[86:89], v[46:49], v[54:57]
	v_mfma_f32_16x16x32_f16 v[30:33], v[94:97], v[46:49], v[30:33]
	ds_read_b128 v[46:49], v6
	ds_read_b128 v[62:65], v6 offset:2048
	ds_read_b128 v[66:69], v6 offset:4096
	ds_read_b128 v[70:73], v6 offset:6144
	ds_read_b128 v[90:93], v8 offset:16384
	ds_read_b128 v[98:101], v8 offset:18432
	v_mfma_f32_16x16x32_f16 v[58:61], v[86:89], v[74:77], v[58:61]
	v_mfma_f32_16x16x32_f16 v[50:53], v[94:97], v[74:77], v[50:53]
	v_mfma_f32_16x16x32_f16 v[34:37], v[86:89], v[78:81], v[34:37]
	v_mfma_f32_16x16x32_f16 v[26:29], v[94:97], v[78:81], v[26:29]
	v_mfma_f32_16x16x32_f16 v[38:41], v[86:89], v[82:85], v[38:41]
	v_mfma_f32_16x16x32_f16 v[42:45], v[94:97], v[82:85], v[42:45]
	s_add_u32 s28, s2, 0x600
	s_mov_b32 m0, s18
	s_waitcnt vmcnt(8) lgkmcnt(0)
	s_barrier
	s_addc_u32 s29, s3, 0
	s_add_u32 s30, s4, 0x600
	global_load_lds_dwordx4 v3, s[28:29]
	s_mov_b32 m0, s15
	s_addc_u32 s31, s5, 0
	global_load_lds_dwordx4 v4, s[28:29]
	s_mov_b32 m0, s16
	s_nop 0
	global_load_lds_dwordx4 v3, s[30:31]
	s_mov_b32 m0, s17
	s_nop 0
	global_load_lds_dwordx4 v4, s[30:31]
	s_waitcnt lgkmcnt(0)
	v_mfma_f32_16x16x32_f16 v[54:57], v[90:93], v[46:49], v[54:57]
	v_mfma_f32_16x16x32_f16 v[30:33], v[98:101], v[46:49], v[30:33]
	ds_read_b128 v[46:49], v7 offset:32768
	ds_read_b128 v[74:77], v7 offset:34816
	ds_read_b128 v[78:81], v7 offset:36864
	ds_read_b128 v[82:85], v7 offset:38912
	ds_read_b128 v[86:89], v5 offset:49152
	ds_read_b128 v[94:97], v5 offset:51200
	v_mfma_f32_16x16x32_f16 v[58:61], v[90:93], v[62:65], v[58:61]
	v_mfma_f32_16x16x32_f16 v[50:53], v[98:101], v[62:65], v[50:53]
	v_mfma_f32_16x16x32_f16 v[34:37], v[90:93], v[66:69], v[34:37]
	v_mfma_f32_16x16x32_f16 v[26:29], v[98:101], v[66:69], v[26:29]
	v_mfma_f32_16x16x32_f16 v[38:41], v[90:93], v[70:73], v[38:41]
	v_mfma_f32_16x16x32_f16 v[42:45], v[98:101], v[70:73], v[42:45]
	s_waitcnt lgkmcnt(0)
	v_mfma_f32_16x16x32_f16 v[54:57], v[86:89], v[46:49], v[54:57]
	v_mfma_f32_16x16x32_f16 v[30:33], v[94:97], v[46:49], v[30:33]
	ds_read_b128 v[46:49], v6 offset:32768
	ds_read_b128 v[62:65], v6 offset:34816
	ds_read_b128 v[66:69], v6 offset:36864
	ds_read_b128 v[70:73], v6 offset:38912
	ds_read_b128 v[90:93], v8 offset:49152
	ds_read_b128 v[98:101], v8 offset:51200
	v_mfma_f32_16x16x32_f16 v[58:61], v[86:89], v[74:77], v[58:61]
	v_mfma_f32_16x16x32_f16 v[50:53], v[94:97], v[74:77], v[50:53]
	v_mfma_f32_16x16x32_f16 v[34:37], v[86:89], v[78:81], v[34:37]
	v_mfma_f32_16x16x32_f16 v[26:29], v[94:97], v[78:81], v[26:29]
	v_mfma_f32_16x16x32_f16 v[38:41], v[86:89], v[82:85], v[38:41]
	v_mfma_f32_16x16x32_f16 v[42:45], v[94:97], v[82:85], v[42:45]
	s_add_u32 s28, s2, 0x680
	s_mov_b32 m0, s14
	s_waitcnt vmcnt(8) lgkmcnt(0)
	s_barrier
	s_addc_u32 s29, s3, 0
	s_add_u32 s30, s4, 0x680
	global_load_lds_dwordx4 v3, s[28:29]
	s_mov_b32 m0, s6
	s_addc_u32 s31, s5, 0
	global_load_lds_dwordx4 v4, s[28:29]
	s_mov_b32 m0, s7
	s_nop 0
	global_load_lds_dwordx4 v3, s[30:31]
	s_mov_b32 m0, s10
	s_nop 0
	global_load_lds_dwordx4 v4, s[30:31]
	s_waitcnt lgkmcnt(0)
	v_mfma_f32_16x16x32_f16 v[54:57], v[90:93], v[46:49], v[54:57]
	v_mfma_f32_16x16x32_f16 v[30:33], v[98:101], v[46:49], v[30:33]
	ds_read_b128 v[46:49], v9
	ds_read_b128 v[74:77], v10
	ds_read_b128 v[78:81], v11
	ds_read_b128 v[82:85], v12
	ds_read_b128 v[86:89], v13
	ds_read_b128 v[94:97], v14
	v_mfma_f32_16x16x32_f16 v[58:61], v[90:93], v[62:65], v[58:61]
	v_mfma_f32_16x16x32_f16 v[50:53], v[98:101], v[62:65], v[50:53]
	v_mfma_f32_16x16x32_f16 v[34:37], v[90:93], v[66:69], v[34:37]
	v_mfma_f32_16x16x32_f16 v[26:29], v[98:101], v[66:69], v[26:29]
	v_mfma_f32_16x16x32_f16 v[38:41], v[90:93], v[70:73], v[38:41]
	v_mfma_f32_16x16x32_f16 v[42:45], v[98:101], v[70:73], v[42:45]
	s_waitcnt lgkmcnt(0)
	v_mfma_f32_16x16x32_f16 v[54:57], v[86:89], v[46:49], v[54:57]
	v_mfma_f32_16x16x32_f16 v[30:33], v[94:97], v[46:49], v[30:33]
	ds_read_b128 v[46:49], v15
	ds_read_b128 v[62:65], v15 offset:2048
	ds_read_b128 v[66:69], v15 offset:4096
	ds_read_b128 v[70:73], v15 offset:6144
	ds_read_b128 v[90:93], v16
	ds_read_b128 v[98:101], v16 offset:2048
	v_mfma_f32_16x16x32_f16 v[58:61], v[86:89], v[74:77], v[58:61]
	v_mfma_f32_16x16x32_f16 v[50:53], v[94:97], v[74:77], v[50:53]
	v_mfma_f32_16x16x32_f16 v[34:37], v[86:89], v[78:81], v[34:37]
	v_mfma_f32_16x16x32_f16 v[26:29], v[94:97], v[78:81], v[26:29]
	v_mfma_f32_16x16x32_f16 v[38:41], v[86:89], v[82:85], v[38:41]
	v_mfma_f32_16x16x32_f16 v[42:45], v[94:97], v[82:85], v[42:45]
	s_add_u32 s28, s2, 0x700
	s_mov_b32 m0, s22
	s_waitcnt vmcnt(8) lgkmcnt(0)
	s_barrier
	s_addc_u32 s29, s3, 0
	s_add_u32 s30, s4, 0x700
	global_load_lds_dwordx4 v3, s[28:29]
	s_mov_b32 m0, s19
	s_addc_u32 s31, s5, 0
	global_load_lds_dwordx4 v4, s[28:29]
	s_mov_b32 m0, s20
	s_nop 0
	global_load_lds_dwordx4 v3, s[30:31]
	s_mov_b32 m0, s21
	s_nop 0
	global_load_lds_dwordx4 v4, s[30:31]
	s_waitcnt lgkmcnt(0)
	v_mfma_f32_16x16x32_f16 v[54:57], v[90:93], v[46:49], v[54:57]
	v_mfma_f32_16x16x32_f16 v[30:33], v[98:101], v[46:49], v[30:33]
	ds_read_b128 v[46:49], v17
	ds_read_b128 v[74:77], v18
	ds_read_b128 v[78:81], v19
	ds_read_b128 v[82:85], v20
	ds_read_b128 v[86:89], v21
	ds_read_b128 v[94:97], v22
	v_mfma_f32_16x16x32_f16 v[58:61], v[90:93], v[62:65], v[58:61]
	v_mfma_f32_16x16x32_f16 v[50:53], v[98:101], v[62:65], v[50:53]
	v_mfma_f32_16x16x32_f16 v[34:37], v[90:93], v[66:69], v[34:37]
	v_mfma_f32_16x16x32_f16 v[26:29], v[98:101], v[66:69], v[26:29]
	v_mfma_f32_16x16x32_f16 v[38:41], v[90:93], v[70:73], v[38:41]
	v_mfma_f32_16x16x32_f16 v[42:45], v[98:101], v[70:73], v[42:45]
	s_waitcnt lgkmcnt(0)
	v_mfma_f32_16x16x32_f16 v[54:57], v[86:89], v[46:49], v[54:57]
	v_mfma_f32_16x16x32_f16 v[30:33], v[94:97], v[46:49], v[30:33]
	ds_read_b128 v[46:49], v23
	ds_read_b128 v[62:65], v23 offset:2048
	ds_read_b128 v[66:69], v23 offset:4096
	ds_read_b128 v[70:73], v23 offset:6144
	ds_read_b128 v[90:93], v24
	ds_read_b128 v[98:101], v24 offset:2048
	v_mfma_f32_16x16x32_f16 v[58:61], v[86:89], v[74:77], v[58:61]
	v_mfma_f32_16x16x32_f16 v[50:53], v[94:97], v[74:77], v[50:53]
	v_mfma_f32_16x16x32_f16 v[34:37], v[86:89], v[78:81], v[34:37]
	v_mfma_f32_16x16x32_f16 v[26:29], v[94:97], v[78:81], v[26:29]
	v_mfma_f32_16x16x32_f16 v[38:41], v[86:89], v[82:85], v[38:41]
	v_mfma_f32_16x16x32_f16 v[42:45], v[94:97], v[82:85], v[42:45]
	s_add_u32 s28, s2, 0x780
	s_mov_b32 m0, s26
	s_waitcnt vmcnt(8) lgkmcnt(0)
	s_barrier
	s_addc_u32 s29, s3, 0
	s_add_u32 s30, s4, 0x780
	global_load_lds_dwordx4 v3, s[28:29]
	s_mov_b32 m0, s23
	s_addc_u32 s31, s5, 0
	global_load_lds_dwordx4 v4, s[28:29]
	s_mov_b32 m0, s24
	s_nop 0
	global_load_lds_dwordx4 v3, s[30:31]
	s_mov_b32 m0, s25
	s_nop 0
	global_load_lds_dwordx4 v4, s[30:31]
	s_waitcnt lgkmcnt(0)
	v_mfma_f32_16x16x32_f16 v[54:57], v[90:93], v[46:49], v[54:57]
	v_mfma_f32_16x16x32_f16 v[30:33], v[98:101], v[46:49], v[30:33]
	ds_read_b128 v[46:49], v7
	ds_read_b128 v[74:77], v7 offset:2048
	ds_read_b128 v[78:81], v7 offset:4096
	ds_read_b128 v[82:85], v7 offset:6144
	ds_read_b128 v[86:89], v5 offset:16384
	ds_read_b128 v[94:97], v5 offset:18432
	v_mfma_f32_16x16x32_f16 v[58:61], v[90:93], v[62:65], v[58:61]
	v_mfma_f32_16x16x32_f16 v[50:53], v[98:101], v[62:65], v[50:53]
	v_mfma_f32_16x16x32_f16 v[34:37], v[90:93], v[66:69], v[34:37]
	v_mfma_f32_16x16x32_f16 v[26:29], v[98:101], v[66:69], v[26:29]
	v_mfma_f32_16x16x32_f16 v[38:41], v[90:93], v[70:73], v[38:41]
	v_mfma_f32_16x16x32_f16 v[42:45], v[98:101], v[70:73], v[42:45]
	s_waitcnt lgkmcnt(0)
	v_mfma_f32_16x16x32_f16 v[54:57], v[86:89], v[46:49], v[54:57]
	v_mfma_f32_16x16x32_f16 v[30:33], v[94:97], v[46:49], v[30:33]
	ds_read_b128 v[46:49], v6
	ds_read_b128 v[62:65], v6 offset:2048
	ds_read_b128 v[66:69], v6 offset:4096
	ds_read_b128 v[70:73], v6 offset:6144
	ds_read_b128 v[90:93], v8 offset:16384
	ds_read_b128 v[98:101], v8 offset:18432
	v_mfma_f32_16x16x32_f16 v[58:61], v[86:89], v[74:77], v[58:61]
	v_mfma_f32_16x16x32_f16 v[50:53], v[94:97], v[74:77], v[50:53]
	v_mfma_f32_16x16x32_f16 v[34:37], v[86:89], v[78:81], v[34:37]
	v_mfma_f32_16x16x32_f16 v[26:29], v[94:97], v[78:81], v[26:29]
	v_mfma_f32_16x16x32_f16 v[38:41], v[86:89], v[82:85], v[38:41]
	v_mfma_f32_16x16x32_f16 v[42:45], v[94:97], v[82:85], v[42:45]
	s_add_u32 s28, s2, 0x800
	s_mov_b32 m0, s18
	s_waitcnt vmcnt(8) lgkmcnt(0)
	s_barrier
	s_addc_u32 s29, s3, 0
	s_add_u32 s30, s4, 0x800
	global_load_lds_dwordx4 v3, s[28:29]
	s_mov_b32 m0, s15
	s_addc_u32 s31, s5, 0
	global_load_lds_dwordx4 v4, s[28:29]
	s_mov_b32 m0, s16
	s_nop 0
	global_load_lds_dwordx4 v3, s[30:31]
	s_mov_b32 m0, s17
	s_nop 0
	global_load_lds_dwordx4 v4, s[30:31]
	s_waitcnt lgkmcnt(0)
	v_mfma_f32_16x16x32_f16 v[54:57], v[90:93], v[46:49], v[54:57]
	v_mfma_f32_16x16x32_f16 v[30:33], v[98:101], v[46:49], v[30:33]
	ds_read_b128 v[46:49], v7 offset:32768
	ds_read_b128 v[74:77], v7 offset:34816
	ds_read_b128 v[78:81], v7 offset:36864
	ds_read_b128 v[82:85], v7 offset:38912
	ds_read_b128 v[86:89], v5 offset:49152
	ds_read_b128 v[94:97], v5 offset:51200
	v_mfma_f32_16x16x32_f16 v[58:61], v[90:93], v[62:65], v[58:61]
	v_mfma_f32_16x16x32_f16 v[50:53], v[98:101], v[62:65], v[50:53]
	v_mfma_f32_16x16x32_f16 v[34:37], v[90:93], v[66:69], v[34:37]
	v_mfma_f32_16x16x32_f16 v[26:29], v[98:101], v[66:69], v[26:29]
	v_mfma_f32_16x16x32_f16 v[38:41], v[90:93], v[70:73], v[38:41]
	v_mfma_f32_16x16x32_f16 v[42:45], v[98:101], v[70:73], v[42:45]
	s_waitcnt lgkmcnt(0)
	v_mfma_f32_16x16x32_f16 v[54:57], v[86:89], v[46:49], v[54:57]
	v_mfma_f32_16x16x32_f16 v[30:33], v[94:97], v[46:49], v[30:33]
	ds_read_b128 v[46:49], v6 offset:32768
	ds_read_b128 v[62:65], v6 offset:34816
	ds_read_b128 v[66:69], v6 offset:36864
	ds_read_b128 v[70:73], v6 offset:38912
	ds_read_b128 v[90:93], v8 offset:49152
	ds_read_b128 v[98:101], v8 offset:51200
	v_mfma_f32_16x16x32_f16 v[58:61], v[86:89], v[74:77], v[58:61]
	v_mfma_f32_16x16x32_f16 v[50:53], v[94:97], v[74:77], v[50:53]
	v_mfma_f32_16x16x32_f16 v[34:37], v[86:89], v[78:81], v[34:37]
	v_mfma_f32_16x16x32_f16 v[26:29], v[94:97], v[78:81], v[26:29]
	v_mfma_f32_16x16x32_f16 v[38:41], v[86:89], v[82:85], v[38:41]
	v_mfma_f32_16x16x32_f16 v[42:45], v[94:97], v[82:85], v[42:45]
	s_add_u32 s28, s2, 0x880
	s_mov_b32 m0, s14
	s_waitcnt vmcnt(8) lgkmcnt(0)
	s_barrier
	s_addc_u32 s29, s3, 0
	s_add_u32 s30, s4, 0x880
	global_load_lds_dwordx4 v3, s[28:29]
	s_mov_b32 m0, s6
	s_addc_u32 s31, s5, 0
	global_load_lds_dwordx4 v4, s[28:29]
	s_mov_b32 m0, s7
	s_nop 0
	global_load_lds_dwordx4 v3, s[30:31]
	s_mov_b32 m0, s10
	s_nop 0
	global_load_lds_dwordx4 v4, s[30:31]
	s_waitcnt lgkmcnt(0)
	v_mfma_f32_16x16x32_f16 v[54:57], v[90:93], v[46:49], v[54:57]
	v_mfma_f32_16x16x32_f16 v[30:33], v[98:101], v[46:49], v[30:33]
	ds_read_b128 v[46:49], v9
	ds_read_b128 v[74:77], v10
	ds_read_b128 v[78:81], v11
	ds_read_b128 v[82:85], v12
	ds_read_b128 v[86:89], v13
	ds_read_b128 v[94:97], v14
	v_mfma_f32_16x16x32_f16 v[58:61], v[90:93], v[62:65], v[58:61]
	v_mfma_f32_16x16x32_f16 v[50:53], v[98:101], v[62:65], v[50:53]
	v_mfma_f32_16x16x32_f16 v[34:37], v[90:93], v[66:69], v[34:37]
	v_mfma_f32_16x16x32_f16 v[26:29], v[98:101], v[66:69], v[26:29]
	v_mfma_f32_16x16x32_f16 v[38:41], v[90:93], v[70:73], v[38:41]
	v_mfma_f32_16x16x32_f16 v[42:45], v[98:101], v[70:73], v[42:45]
	s_waitcnt lgkmcnt(0)
	v_mfma_f32_16x16x32_f16 v[54:57], v[86:89], v[46:49], v[54:57]
	v_mfma_f32_16x16x32_f16 v[30:33], v[94:97], v[46:49], v[30:33]
	ds_read_b128 v[46:49], v15
	ds_read_b128 v[62:65], v15 offset:2048
	ds_read_b128 v[66:69], v15 offset:4096
	ds_read_b128 v[70:73], v15 offset:6144
	ds_read_b128 v[90:93], v16
	ds_read_b128 v[98:101], v16 offset:2048
	v_mfma_f32_16x16x32_f16 v[58:61], v[86:89], v[74:77], v[58:61]
	v_mfma_f32_16x16x32_f16 v[50:53], v[94:97], v[74:77], v[50:53]
	v_mfma_f32_16x16x32_f16 v[34:37], v[86:89], v[78:81], v[34:37]
	v_mfma_f32_16x16x32_f16 v[26:29], v[94:97], v[78:81], v[26:29]
	v_mfma_f32_16x16x32_f16 v[38:41], v[86:89], v[82:85], v[38:41]
	v_mfma_f32_16x16x32_f16 v[42:45], v[94:97], v[82:85], v[42:45]
	s_add_u32 s28, s2, 0x900
	s_mov_b32 m0, s22
	s_waitcnt vmcnt(8) lgkmcnt(0)
	s_barrier
	s_addc_u32 s29, s3, 0
	s_add_u32 s30, s4, 0x900
	global_load_lds_dwordx4 v3, s[28:29]
	s_mov_b32 m0, s19
	s_addc_u32 s31, s5, 0
	global_load_lds_dwordx4 v4, s[28:29]
	s_mov_b32 m0, s20
	s_nop 0
	global_load_lds_dwordx4 v3, s[30:31]
	s_mov_b32 m0, s21
	s_nop 0
	global_load_lds_dwordx4 v4, s[30:31]
	s_waitcnt lgkmcnt(0)
	v_mfma_f32_16x16x32_f16 v[54:57], v[90:93], v[46:49], v[54:57]
	v_mfma_f32_16x16x32_f16 v[30:33], v[98:101], v[46:49], v[30:33]
	ds_read_b128 v[46:49], v17
	ds_read_b128 v[74:77], v18
	ds_read_b128 v[78:81], v19
	ds_read_b128 v[82:85], v20
	ds_read_b128 v[86:89], v21
	ds_read_b128 v[94:97], v22
	v_mfma_f32_16x16x32_f16 v[58:61], v[90:93], v[62:65], v[58:61]
	v_mfma_f32_16x16x32_f16 v[50:53], v[98:101], v[62:65], v[50:53]
	v_mfma_f32_16x16x32_f16 v[34:37], v[90:93], v[66:69], v[34:37]
	v_mfma_f32_16x16x32_f16 v[26:29], v[98:101], v[66:69], v[26:29]
	v_mfma_f32_16x16x32_f16 v[38:41], v[90:93], v[70:73], v[38:41]
	v_mfma_f32_16x16x32_f16 v[42:45], v[98:101], v[70:73], v[42:45]
	s_waitcnt lgkmcnt(0)
	v_mfma_f32_16x16x32_f16 v[54:57], v[86:89], v[46:49], v[54:57]
	v_mfma_f32_16x16x32_f16 v[30:33], v[94:97], v[46:49], v[30:33]
	ds_read_b128 v[46:49], v23
	ds_read_b128 v[62:65], v23 offset:2048
	ds_read_b128 v[66:69], v23 offset:4096
	ds_read_b128 v[70:73], v23 offset:6144
	ds_read_b128 v[90:93], v24
	ds_read_b128 v[98:101], v24 offset:2048
	v_mfma_f32_16x16x32_f16 v[58:61], v[86:89], v[74:77], v[58:61]
	v_mfma_f32_16x16x32_f16 v[50:53], v[94:97], v[74:77], v[50:53]
	v_mfma_f32_16x16x32_f16 v[34:37], v[86:89], v[78:81], v[34:37]
	v_mfma_f32_16x16x32_f16 v[26:29], v[94:97], v[78:81], v[26:29]
	v_mfma_f32_16x16x32_f16 v[38:41], v[86:89], v[82:85], v[38:41]
	v_mfma_f32_16x16x32_f16 v[42:45], v[94:97], v[82:85], v[42:45]
	s_add_u32 s28, s2, 0x980
	s_mov_b32 m0, s26
	s_waitcnt vmcnt(8) lgkmcnt(0)
	s_barrier
	s_addc_u32 s29, s3, 0
	s_add_u32 s30, s4, 0x980
	global_load_lds_dwordx4 v3, s[28:29]
	s_mov_b32 m0, s23
	s_addc_u32 s31, s5, 0
	global_load_lds_dwordx4 v4, s[28:29]
	s_mov_b32 m0, s24
	s_nop 0
	global_load_lds_dwordx4 v3, s[30:31]
	s_mov_b32 m0, s25
	s_nop 0
	global_load_lds_dwordx4 v4, s[30:31]
	s_waitcnt lgkmcnt(0)
	v_mfma_f32_16x16x32_f16 v[54:57], v[90:93], v[46:49], v[54:57]
	v_mfma_f32_16x16x32_f16 v[30:33], v[98:101], v[46:49], v[30:33]
	ds_read_b128 v[46:49], v7
	ds_read_b128 v[74:77], v7 offset:2048
	ds_read_b128 v[78:81], v7 offset:4096
	ds_read_b128 v[82:85], v7 offset:6144
	ds_read_b128 v[86:89], v5 offset:16384
	ds_read_b128 v[94:97], v5 offset:18432
	v_mfma_f32_16x16x32_f16 v[58:61], v[90:93], v[62:65], v[58:61]
	v_mfma_f32_16x16x32_f16 v[50:53], v[98:101], v[62:65], v[50:53]
	v_mfma_f32_16x16x32_f16 v[34:37], v[90:93], v[66:69], v[34:37]
	v_mfma_f32_16x16x32_f16 v[26:29], v[98:101], v[66:69], v[26:29]
	v_mfma_f32_16x16x32_f16 v[38:41], v[90:93], v[70:73], v[38:41]
	v_mfma_f32_16x16x32_f16 v[42:45], v[98:101], v[70:73], v[42:45]
	s_waitcnt lgkmcnt(0)
	v_mfma_f32_16x16x32_f16 v[54:57], v[86:89], v[46:49], v[54:57]
	v_mfma_f32_16x16x32_f16 v[30:33], v[94:97], v[46:49], v[30:33]
	ds_read_b128 v[46:49], v6
	ds_read_b128 v[62:65], v6 offset:2048
	ds_read_b128 v[66:69], v6 offset:4096
	ds_read_b128 v[70:73], v6 offset:6144
	ds_read_b128 v[90:93], v8 offset:16384
	ds_read_b128 v[98:101], v8 offset:18432
	v_mfma_f32_16x16x32_f16 v[58:61], v[86:89], v[74:77], v[58:61]
	v_mfma_f32_16x16x32_f16 v[50:53], v[94:97], v[74:77], v[50:53]
	v_mfma_f32_16x16x32_f16 v[34:37], v[86:89], v[78:81], v[34:37]
	v_mfma_f32_16x16x32_f16 v[26:29], v[94:97], v[78:81], v[26:29]
	v_mfma_f32_16x16x32_f16 v[38:41], v[86:89], v[82:85], v[38:41]
	v_mfma_f32_16x16x32_f16 v[42:45], v[94:97], v[82:85], v[42:45]
	s_add_u32 s28, s2, 0xa00
	s_mov_b32 m0, s18
	s_waitcnt vmcnt(8) lgkmcnt(0)
	s_barrier
	s_addc_u32 s29, s3, 0
	s_add_u32 s30, s4, 0xa00
	global_load_lds_dwordx4 v3, s[28:29]
	s_mov_b32 m0, s15
	s_addc_u32 s31, s5, 0
	global_load_lds_dwordx4 v4, s[28:29]
	s_mov_b32 m0, s16
	s_nop 0
	global_load_lds_dwordx4 v3, s[30:31]
	s_mov_b32 m0, s17
	s_nop 0
	global_load_lds_dwordx4 v4, s[30:31]
	s_waitcnt lgkmcnt(0)
	v_mfma_f32_16x16x32_f16 v[54:57], v[90:93], v[46:49], v[54:57]
	v_mfma_f32_16x16x32_f16 v[30:33], v[98:101], v[46:49], v[30:33]
	ds_read_b128 v[46:49], v7 offset:32768
	ds_read_b128 v[74:77], v7 offset:34816
	ds_read_b128 v[78:81], v7 offset:36864
	ds_read_b128 v[82:85], v7 offset:38912
	ds_read_b128 v[86:89], v5 offset:49152
	ds_read_b128 v[94:97], v5 offset:51200
	v_mfma_f32_16x16x32_f16 v[58:61], v[90:93], v[62:65], v[58:61]
	v_mfma_f32_16x16x32_f16 v[50:53], v[98:101], v[62:65], v[50:53]
	v_mfma_f32_16x16x32_f16 v[34:37], v[90:93], v[66:69], v[34:37]
	v_mfma_f32_16x16x32_f16 v[26:29], v[98:101], v[66:69], v[26:29]
	v_mfma_f32_16x16x32_f16 v[38:41], v[90:93], v[70:73], v[38:41]
	v_mfma_f32_16x16x32_f16 v[42:45], v[98:101], v[70:73], v[42:45]
	s_waitcnt lgkmcnt(0)
	v_mfma_f32_16x16x32_f16 v[54:57], v[86:89], v[46:49], v[54:57]
	v_mfma_f32_16x16x32_f16 v[30:33], v[94:97], v[46:49], v[30:33]
	ds_read_b128 v[46:49], v6 offset:32768
	ds_read_b128 v[62:65], v6 offset:34816
	ds_read_b128 v[66:69], v6 offset:36864
	ds_read_b128 v[70:73], v6 offset:38912
	ds_read_b128 v[90:93], v8 offset:49152
	ds_read_b128 v[98:101], v8 offset:51200
	v_mfma_f32_16x16x32_f16 v[58:61], v[86:89], v[74:77], v[58:61]
	v_mfma_f32_16x16x32_f16 v[50:53], v[94:97], v[74:77], v[50:53]
	v_mfma_f32_16x16x32_f16 v[34:37], v[86:89], v[78:81], v[34:37]
	v_mfma_f32_16x16x32_f16 v[26:29], v[94:97], v[78:81], v[26:29]
	v_mfma_f32_16x16x32_f16 v[38:41], v[86:89], v[82:85], v[38:41]
	v_mfma_f32_16x16x32_f16 v[42:45], v[94:97], v[82:85], v[42:45]
	s_add_u32 s28, s2, 0xa80
	s_mov_b32 m0, s14
	s_waitcnt vmcnt(8) lgkmcnt(0)
	s_barrier
	s_addc_u32 s29, s3, 0
	s_add_u32 s30, s4, 0xa80
	global_load_lds_dwordx4 v3, s[28:29]
	s_mov_b32 m0, s6
	s_addc_u32 s31, s5, 0
	global_load_lds_dwordx4 v4, s[28:29]
	s_mov_b32 m0, s7
	s_nop 0
	global_load_lds_dwordx4 v3, s[30:31]
	s_mov_b32 m0, s10
	s_nop 0
	global_load_lds_dwordx4 v4, s[30:31]
	s_waitcnt lgkmcnt(0)
	v_mfma_f32_16x16x32_f16 v[54:57], v[90:93], v[46:49], v[54:57]
	v_mfma_f32_16x16x32_f16 v[30:33], v[98:101], v[46:49], v[30:33]
	ds_read_b128 v[46:49], v9
	ds_read_b128 v[74:77], v10
	ds_read_b128 v[78:81], v11
	ds_read_b128 v[82:85], v12
	ds_read_b128 v[86:89], v13
	ds_read_b128 v[94:97], v14
	v_mfma_f32_16x16x32_f16 v[58:61], v[90:93], v[62:65], v[58:61]
	v_mfma_f32_16x16x32_f16 v[50:53], v[98:101], v[62:65], v[50:53]
	v_mfma_f32_16x16x32_f16 v[34:37], v[90:93], v[66:69], v[34:37]
	v_mfma_f32_16x16x32_f16 v[26:29], v[98:101], v[66:69], v[26:29]
	v_mfma_f32_16x16x32_f16 v[38:41], v[90:93], v[70:73], v[38:41]
	v_mfma_f32_16x16x32_f16 v[42:45], v[98:101], v[70:73], v[42:45]
	s_waitcnt lgkmcnt(0)
	v_mfma_f32_16x16x32_f16 v[54:57], v[86:89], v[46:49], v[54:57]
	v_mfma_f32_16x16x32_f16 v[30:33], v[94:97], v[46:49], v[30:33]
	ds_read_b128 v[46:49], v15
	ds_read_b128 v[62:65], v15 offset:2048
	ds_read_b128 v[66:69], v15 offset:4096
	ds_read_b128 v[70:73], v15 offset:6144
	ds_read_b128 v[90:93], v16
	ds_read_b128 v[98:101], v16 offset:2048
	v_mfma_f32_16x16x32_f16 v[58:61], v[86:89], v[74:77], v[58:61]
	v_mfma_f32_16x16x32_f16 v[50:53], v[94:97], v[74:77], v[50:53]
	v_mfma_f32_16x16x32_f16 v[34:37], v[86:89], v[78:81], v[34:37]
	v_mfma_f32_16x16x32_f16 v[26:29], v[94:97], v[78:81], v[26:29]
	v_mfma_f32_16x16x32_f16 v[38:41], v[86:89], v[82:85], v[38:41]
	v_mfma_f32_16x16x32_f16 v[42:45], v[94:97], v[82:85], v[42:45]
	s_add_u32 s28, s2, 0xb00
	s_mov_b32 m0, s22
	s_waitcnt vmcnt(8) lgkmcnt(0)
	s_barrier
	s_addc_u32 s29, s3, 0
	s_add_u32 s30, s4, 0xb00
	global_load_lds_dwordx4 v3, s[28:29]
	s_mov_b32 m0, s19
	s_addc_u32 s31, s5, 0
	global_load_lds_dwordx4 v4, s[28:29]
	s_mov_b32 m0, s20
	s_nop 0
	global_load_lds_dwordx4 v3, s[30:31]
	s_mov_b32 m0, s21
	s_nop 0
	global_load_lds_dwordx4 v4, s[30:31]
	s_waitcnt lgkmcnt(0)
	v_mfma_f32_16x16x32_f16 v[54:57], v[90:93], v[46:49], v[54:57]
	v_mfma_f32_16x16x32_f16 v[30:33], v[98:101], v[46:49], v[30:33]
	ds_read_b128 v[46:49], v17
	ds_read_b128 v[74:77], v18
	ds_read_b128 v[78:81], v19
	ds_read_b128 v[82:85], v20
	ds_read_b128 v[86:89], v21
	ds_read_b128 v[94:97], v22
	v_mfma_f32_16x16x32_f16 v[58:61], v[90:93], v[62:65], v[58:61]
	v_mfma_f32_16x16x32_f16 v[50:53], v[98:101], v[62:65], v[50:53]
	v_mfma_f32_16x16x32_f16 v[34:37], v[90:93], v[66:69], v[34:37]
	v_mfma_f32_16x16x32_f16 v[26:29], v[98:101], v[66:69], v[26:29]
	v_mfma_f32_16x16x32_f16 v[38:41], v[90:93], v[70:73], v[38:41]
	v_mfma_f32_16x16x32_f16 v[42:45], v[98:101], v[70:73], v[42:45]
	s_waitcnt lgkmcnt(0)
	v_mfma_f32_16x16x32_f16 v[54:57], v[86:89], v[46:49], v[54:57]
	v_mfma_f32_16x16x32_f16 v[30:33], v[94:97], v[46:49], v[30:33]
	ds_read_b128 v[46:49], v23
	ds_read_b128 v[62:65], v23 offset:2048
	ds_read_b128 v[66:69], v23 offset:4096
	ds_read_b128 v[70:73], v23 offset:6144
	ds_read_b128 v[90:93], v24
	ds_read_b128 v[98:101], v24 offset:2048
	v_mfma_f32_16x16x32_f16 v[58:61], v[86:89], v[74:77], v[58:61]
	v_mfma_f32_16x16x32_f16 v[50:53], v[94:97], v[74:77], v[50:53]
	v_mfma_f32_16x16x32_f16 v[34:37], v[86:89], v[78:81], v[34:37]
	v_mfma_f32_16x16x32_f16 v[26:29], v[94:97], v[78:81], v[26:29]
	v_mfma_f32_16x16x32_f16 v[38:41], v[86:89], v[82:85], v[38:41]
	v_mfma_f32_16x16x32_f16 v[42:45], v[94:97], v[82:85], v[42:45]
	s_add_u32 s28, s2, 0xb80
	s_mov_b32 m0, s26
	s_waitcnt vmcnt(8) lgkmcnt(0)
	s_barrier
	s_addc_u32 s29, s3, 0
	s_add_u32 s30, s4, 0xb80
	global_load_lds_dwordx4 v3, s[28:29]
	s_mov_b32 m0, s23
	s_addc_u32 s31, s5, 0
	global_load_lds_dwordx4 v4, s[28:29]
	s_mov_b32 m0, s24
	s_nop 0
	global_load_lds_dwordx4 v3, s[30:31]
	s_mov_b32 m0, s25
	s_nop 0
	global_load_lds_dwordx4 v4, s[30:31]
	s_waitcnt lgkmcnt(0)
	v_mfma_f32_16x16x32_f16 v[54:57], v[90:93], v[46:49], v[54:57]
	v_mfma_f32_16x16x32_f16 v[30:33], v[98:101], v[46:49], v[30:33]
	ds_read_b128 v[46:49], v7
	ds_read_b128 v[74:77], v7 offset:2048
	ds_read_b128 v[78:81], v7 offset:4096
	ds_read_b128 v[82:85], v7 offset:6144
	ds_read_b128 v[86:89], v5 offset:16384
	ds_read_b128 v[94:97], v5 offset:18432
	v_mfma_f32_16x16x32_f16 v[58:61], v[90:93], v[62:65], v[58:61]
	v_mfma_f32_16x16x32_f16 v[50:53], v[98:101], v[62:65], v[50:53]
	v_mfma_f32_16x16x32_f16 v[34:37], v[90:93], v[66:69], v[34:37]
	v_mfma_f32_16x16x32_f16 v[26:29], v[98:101], v[66:69], v[26:29]
	v_mfma_f32_16x16x32_f16 v[38:41], v[90:93], v[70:73], v[38:41]
	v_mfma_f32_16x16x32_f16 v[42:45], v[98:101], v[70:73], v[42:45]
	s_waitcnt lgkmcnt(0)
	v_mfma_f32_16x16x32_f16 v[54:57], v[86:89], v[46:49], v[54:57]
	v_mfma_f32_16x16x32_f16 v[30:33], v[94:97], v[46:49], v[30:33]
	ds_read_b128 v[46:49], v6
	ds_read_b128 v[62:65], v6 offset:2048
	ds_read_b128 v[66:69], v6 offset:4096
	ds_read_b128 v[70:73], v6 offset:6144
	ds_read_b128 v[90:93], v8 offset:16384
	ds_read_b128 v[98:101], v8 offset:18432
	v_mfma_f32_16x16x32_f16 v[58:61], v[86:89], v[74:77], v[58:61]
	v_mfma_f32_16x16x32_f16 v[50:53], v[94:97], v[74:77], v[50:53]
	v_mfma_f32_16x16x32_f16 v[34:37], v[86:89], v[78:81], v[34:37]
	v_mfma_f32_16x16x32_f16 v[26:29], v[94:97], v[78:81], v[26:29]
	v_mfma_f32_16x16x32_f16 v[38:41], v[86:89], v[82:85], v[38:41]
	v_mfma_f32_16x16x32_f16 v[42:45], v[94:97], v[82:85], v[42:45]
	s_add_u32 s28, s2, 0xc00
	s_mov_b32 m0, s18
	s_waitcnt vmcnt(8) lgkmcnt(0)
	s_barrier
	s_addc_u32 s29, s3, 0
	s_add_u32 s30, s4, 0xc00
	global_load_lds_dwordx4 v3, s[28:29]
	s_mov_b32 m0, s15
	s_addc_u32 s31, s5, 0
	global_load_lds_dwordx4 v4, s[28:29]
	s_mov_b32 m0, s16
	s_nop 0
	global_load_lds_dwordx4 v3, s[30:31]
	s_mov_b32 m0, s17
	s_nop 0
	global_load_lds_dwordx4 v4, s[30:31]
	s_waitcnt lgkmcnt(0)
	v_mfma_f32_16x16x32_f16 v[54:57], v[90:93], v[46:49], v[54:57]
	v_mfma_f32_16x16x32_f16 v[30:33], v[98:101], v[46:49], v[30:33]
	ds_read_b128 v[46:49], v7 offset:32768
	ds_read_b128 v[74:77], v7 offset:34816
	ds_read_b128 v[78:81], v7 offset:36864
	ds_read_b128 v[82:85], v7 offset:38912
	ds_read_b128 v[86:89], v5 offset:49152
	ds_read_b128 v[94:97], v5 offset:51200
	v_mfma_f32_16x16x32_f16 v[58:61], v[90:93], v[62:65], v[58:61]
	v_mfma_f32_16x16x32_f16 v[50:53], v[98:101], v[62:65], v[50:53]
	v_mfma_f32_16x16x32_f16 v[34:37], v[90:93], v[66:69], v[34:37]
	v_mfma_f32_16x16x32_f16 v[26:29], v[98:101], v[66:69], v[26:29]
	v_mfma_f32_16x16x32_f16 v[38:41], v[90:93], v[70:73], v[38:41]
	v_mfma_f32_16x16x32_f16 v[42:45], v[98:101], v[70:73], v[42:45]
	s_waitcnt lgkmcnt(0)
	v_mfma_f32_16x16x32_f16 v[54:57], v[86:89], v[46:49], v[54:57]
	v_mfma_f32_16x16x32_f16 v[30:33], v[94:97], v[46:49], v[30:33]
	ds_read_b128 v[46:49], v6 offset:32768
	ds_read_b128 v[62:65], v6 offset:34816
	ds_read_b128 v[66:69], v6 offset:36864
	ds_read_b128 v[70:73], v6 offset:38912
	ds_read_b128 v[90:93], v8 offset:49152
	ds_read_b128 v[98:101], v8 offset:51200
	v_mfma_f32_16x16x32_f16 v[58:61], v[86:89], v[74:77], v[58:61]
	v_mfma_f32_16x16x32_f16 v[50:53], v[94:97], v[74:77], v[50:53]
	v_mfma_f32_16x16x32_f16 v[34:37], v[86:89], v[78:81], v[34:37]
	v_mfma_f32_16x16x32_f16 v[26:29], v[94:97], v[78:81], v[26:29]
	v_mfma_f32_16x16x32_f16 v[38:41], v[86:89], v[82:85], v[38:41]
	v_mfma_f32_16x16x32_f16 v[42:45], v[94:97], v[82:85], v[42:45]
	s_add_u32 s28, s2, 0xc80
	s_mov_b32 m0, s14
	s_waitcnt vmcnt(8) lgkmcnt(0)
	s_barrier
	s_addc_u32 s29, s3, 0
	s_add_u32 s30, s4, 0xc80
	global_load_lds_dwordx4 v3, s[28:29]
	s_mov_b32 m0, s6
	s_addc_u32 s31, s5, 0
	global_load_lds_dwordx4 v4, s[28:29]
	s_mov_b32 m0, s7
	s_nop 0
	global_load_lds_dwordx4 v3, s[30:31]
	s_mov_b32 m0, s10
	s_nop 0
	global_load_lds_dwordx4 v4, s[30:31]
	s_waitcnt lgkmcnt(0)
	v_mfma_f32_16x16x32_f16 v[54:57], v[90:93], v[46:49], v[54:57]
	v_mfma_f32_16x16x32_f16 v[30:33], v[98:101], v[46:49], v[30:33]
	ds_read_b128 v[46:49], v9
	ds_read_b128 v[74:77], v10
	ds_read_b128 v[78:81], v11
	ds_read_b128 v[82:85], v12
	ds_read_b128 v[86:89], v13
	ds_read_b128 v[94:97], v14
	v_mfma_f32_16x16x32_f16 v[58:61], v[90:93], v[62:65], v[58:61]
	v_mfma_f32_16x16x32_f16 v[50:53], v[98:101], v[62:65], v[50:53]
	v_mfma_f32_16x16x32_f16 v[34:37], v[90:93], v[66:69], v[34:37]
	v_mfma_f32_16x16x32_f16 v[26:29], v[98:101], v[66:69], v[26:29]
	v_mfma_f32_16x16x32_f16 v[38:41], v[90:93], v[70:73], v[38:41]
	v_mfma_f32_16x16x32_f16 v[42:45], v[98:101], v[70:73], v[42:45]
	s_waitcnt lgkmcnt(0)
	v_mfma_f32_16x16x32_f16 v[54:57], v[86:89], v[46:49], v[54:57]
	v_mfma_f32_16x16x32_f16 v[30:33], v[94:97], v[46:49], v[30:33]
	ds_read_b128 v[46:49], v15
	ds_read_b128 v[62:65], v15 offset:2048
	ds_read_b128 v[66:69], v15 offset:4096
	ds_read_b128 v[70:73], v15 offset:6144
	ds_read_b128 v[90:93], v16
	ds_read_b128 v[98:101], v16 offset:2048
	v_mfma_f32_16x16x32_f16 v[58:61], v[86:89], v[74:77], v[58:61]
	v_mfma_f32_16x16x32_f16 v[50:53], v[94:97], v[74:77], v[50:53]
	v_mfma_f32_16x16x32_f16 v[34:37], v[86:89], v[78:81], v[34:37]
	v_mfma_f32_16x16x32_f16 v[26:29], v[94:97], v[78:81], v[26:29]
	v_mfma_f32_16x16x32_f16 v[38:41], v[86:89], v[82:85], v[38:41]
	v_mfma_f32_16x16x32_f16 v[42:45], v[94:97], v[82:85], v[42:45]
	s_add_u32 s28, s2, 0xd00
	s_mov_b32 m0, s22
	s_waitcnt vmcnt(8) lgkmcnt(0)
	s_barrier
	s_addc_u32 s29, s3, 0
	s_add_u32 s30, s4, 0xd00
	global_load_lds_dwordx4 v3, s[28:29]
	s_mov_b32 m0, s19
	s_addc_u32 s31, s5, 0
	global_load_lds_dwordx4 v4, s[28:29]
	s_mov_b32 m0, s20
	s_nop 0
	global_load_lds_dwordx4 v3, s[30:31]
	s_mov_b32 m0, s21
	s_nop 0
	global_load_lds_dwordx4 v4, s[30:31]
	s_waitcnt lgkmcnt(0)
	v_mfma_f32_16x16x32_f16 v[54:57], v[90:93], v[46:49], v[54:57]
	v_mfma_f32_16x16x32_f16 v[30:33], v[98:101], v[46:49], v[30:33]
	ds_read_b128 v[46:49], v17
	ds_read_b128 v[74:77], v18
	ds_read_b128 v[78:81], v19
	ds_read_b128 v[82:85], v20
	ds_read_b128 v[86:89], v21
	ds_read_b128 v[94:97], v22
	v_mfma_f32_16x16x32_f16 v[58:61], v[90:93], v[62:65], v[58:61]
	v_mfma_f32_16x16x32_f16 v[50:53], v[98:101], v[62:65], v[50:53]
	v_mfma_f32_16x16x32_f16 v[34:37], v[90:93], v[66:69], v[34:37]
	v_mfma_f32_16x16x32_f16 v[26:29], v[98:101], v[66:69], v[26:29]
	v_mfma_f32_16x16x32_f16 v[38:41], v[90:93], v[70:73], v[38:41]
	v_mfma_f32_16x16x32_f16 v[42:45], v[98:101], v[70:73], v[42:45]
	s_waitcnt lgkmcnt(0)
	v_mfma_f32_16x16x32_f16 v[54:57], v[86:89], v[46:49], v[54:57]
	v_mfma_f32_16x16x32_f16 v[30:33], v[94:97], v[46:49], v[30:33]
	ds_read_b128 v[46:49], v23
	ds_read_b128 v[62:65], v23 offset:2048
	ds_read_b128 v[66:69], v23 offset:4096
	ds_read_b128 v[70:73], v23 offset:6144
	ds_read_b128 v[90:93], v24
	ds_read_b128 v[98:101], v24 offset:2048
	v_mfma_f32_16x16x32_f16 v[58:61], v[86:89], v[74:77], v[58:61]
	v_mfma_f32_16x16x32_f16 v[50:53], v[94:97], v[74:77], v[50:53]
	v_mfma_f32_16x16x32_f16 v[34:37], v[86:89], v[78:81], v[34:37]
	v_mfma_f32_16x16x32_f16 v[26:29], v[94:97], v[78:81], v[26:29]
	v_mfma_f32_16x16x32_f16 v[38:41], v[86:89], v[82:85], v[38:41]
	v_mfma_f32_16x16x32_f16 v[42:45], v[94:97], v[82:85], v[42:45]
	s_add_u32 s28, s2, 0xd80
	s_mov_b32 m0, s26
	s_waitcnt vmcnt(8) lgkmcnt(0)
	s_barrier
	s_addc_u32 s29, s3, 0
	s_add_u32 s30, s4, 0xd80
	global_load_lds_dwordx4 v3, s[28:29]
	s_mov_b32 m0, s23
	s_addc_u32 s31, s5, 0
	global_load_lds_dwordx4 v4, s[28:29]
	s_mov_b32 m0, s24
	s_nop 0
	global_load_lds_dwordx4 v3, s[30:31]
	s_mov_b32 m0, s25
	s_nop 0
	global_load_lds_dwordx4 v4, s[30:31]
	s_waitcnt lgkmcnt(0)
	v_mfma_f32_16x16x32_f16 v[54:57], v[90:93], v[46:49], v[54:57]
	v_mfma_f32_16x16x32_f16 v[30:33], v[98:101], v[46:49], v[30:33]
	ds_read_b128 v[46:49], v7
	ds_read_b128 v[74:77], v7 offset:2048
	ds_read_b128 v[78:81], v7 offset:4096
	ds_read_b128 v[82:85], v7 offset:6144
	ds_read_b128 v[86:89], v5 offset:16384
	ds_read_b128 v[94:97], v5 offset:18432
	v_mfma_f32_16x16x32_f16 v[58:61], v[90:93], v[62:65], v[58:61]
	v_mfma_f32_16x16x32_f16 v[50:53], v[98:101], v[62:65], v[50:53]
	v_mfma_f32_16x16x32_f16 v[34:37], v[90:93], v[66:69], v[34:37]
	v_mfma_f32_16x16x32_f16 v[26:29], v[98:101], v[66:69], v[26:29]
	v_mfma_f32_16x16x32_f16 v[38:41], v[90:93], v[70:73], v[38:41]
	v_mfma_f32_16x16x32_f16 v[42:45], v[98:101], v[70:73], v[42:45]
	s_waitcnt lgkmcnt(0)
	v_mfma_f32_16x16x32_f16 v[54:57], v[86:89], v[46:49], v[54:57]
	v_mfma_f32_16x16x32_f16 v[30:33], v[94:97], v[46:49], v[30:33]
	ds_read_b128 v[46:49], v6
	ds_read_b128 v[62:65], v6 offset:2048
	ds_read_b128 v[66:69], v6 offset:4096
	ds_read_b128 v[70:73], v6 offset:6144
	ds_read_b128 v[90:93], v8 offset:16384
	ds_read_b128 v[98:101], v8 offset:18432
	v_mfma_f32_16x16x32_f16 v[58:61], v[86:89], v[74:77], v[58:61]
	v_mfma_f32_16x16x32_f16 v[50:53], v[94:97], v[74:77], v[50:53]
	v_mfma_f32_16x16x32_f16 v[34:37], v[86:89], v[78:81], v[34:37]
	v_mfma_f32_16x16x32_f16 v[26:29], v[94:97], v[78:81], v[26:29]
	v_mfma_f32_16x16x32_f16 v[38:41], v[86:89], v[82:85], v[38:41]
	v_mfma_f32_16x16x32_f16 v[42:45], v[94:97], v[82:85], v[42:45]
	s_add_u32 s28, s2, 0xe00
	s_mov_b32 m0, s18
	s_waitcnt vmcnt(8) lgkmcnt(0)
	s_barrier
	s_addc_u32 s29, s3, 0
	s_add_u32 s30, s4, 0xe00
	global_load_lds_dwordx4 v3, s[28:29]
	s_mov_b32 m0, s15
	s_addc_u32 s31, s5, 0
	global_load_lds_dwordx4 v4, s[28:29]
	s_mov_b32 m0, s16
	s_nop 0
	global_load_lds_dwordx4 v3, s[30:31]
	s_mov_b32 m0, s17
	s_nop 0
	global_load_lds_dwordx4 v4, s[30:31]
	s_waitcnt lgkmcnt(0)
	v_mfma_f32_16x16x32_f16 v[54:57], v[90:93], v[46:49], v[54:57]
	v_mfma_f32_16x16x32_f16 v[30:33], v[98:101], v[46:49], v[30:33]
	ds_read_b128 v[46:49], v7 offset:32768
	ds_read_b128 v[74:77], v7 offset:34816
	ds_read_b128 v[78:81], v7 offset:36864
	ds_read_b128 v[82:85], v7 offset:38912
	ds_read_b128 v[86:89], v5 offset:49152
	ds_read_b128 v[94:97], v5 offset:51200
	v_mfma_f32_16x16x32_f16 v[58:61], v[90:93], v[62:65], v[58:61]
	v_mfma_f32_16x16x32_f16 v[50:53], v[98:101], v[62:65], v[50:53]
	v_mfma_f32_16x16x32_f16 v[34:37], v[90:93], v[66:69], v[34:37]
	v_mfma_f32_16x16x32_f16 v[26:29], v[98:101], v[66:69], v[26:29]
	v_mfma_f32_16x16x32_f16 v[38:41], v[90:93], v[70:73], v[38:41]
	v_mfma_f32_16x16x32_f16 v[42:45], v[98:101], v[70:73], v[42:45]
	s_waitcnt lgkmcnt(0)
	v_mfma_f32_16x16x32_f16 v[54:57], v[86:89], v[46:49], v[54:57]
	v_mfma_f32_16x16x32_f16 v[30:33], v[94:97], v[46:49], v[30:33]
	ds_read_b128 v[46:49], v6 offset:32768
	ds_read_b128 v[62:65], v6 offset:34816
	ds_read_b128 v[66:69], v6 offset:36864
	ds_read_b128 v[70:73], v6 offset:38912
	ds_read_b128 v[90:93], v8 offset:49152
	ds_read_b128 v[98:101], v8 offset:51200
	v_mfma_f32_16x16x32_f16 v[58:61], v[86:89], v[74:77], v[58:61]
	v_mfma_f32_16x16x32_f16 v[50:53], v[94:97], v[74:77], v[50:53]
	v_mfma_f32_16x16x32_f16 v[34:37], v[86:89], v[78:81], v[34:37]
	v_mfma_f32_16x16x32_f16 v[26:29], v[94:97], v[78:81], v[26:29]
	v_mfma_f32_16x16x32_f16 v[38:41], v[86:89], v[82:85], v[38:41]
	v_mfma_f32_16x16x32_f16 v[42:45], v[94:97], v[82:85], v[42:45]
	s_mov_b32 m0, s14
	s_add_u32 s14, s2, 0xe80
	s_waitcnt vmcnt(8) lgkmcnt(0)
	s_barrier
	s_addc_u32 s15, s3, 0
	s_add_u32 s16, s4, 0xe80
	global_load_lds_dwordx4 v3, s[14:15]
	s_mov_b32 m0, s6
	s_addc_u32 s17, s5, 0
	global_load_lds_dwordx4 v4, s[14:15]
	s_mov_b32 m0, s7
	s_nop 0
	global_load_lds_dwordx4 v3, s[16:17]
	s_mov_b32 m0, s10
	s_nop 0
	global_load_lds_dwordx4 v4, s[16:17]
	s_waitcnt lgkmcnt(0)
	v_mfma_f32_16x16x32_f16 v[54:57], v[90:93], v[46:49], v[54:57]
	v_mfma_f32_16x16x32_f16 v[30:33], v[98:101], v[46:49], v[30:33]
	ds_read_b128 v[46:49], v9
	ds_read_b128 v[74:77], v10
	ds_read_b128 v[78:81], v11
	ds_read_b128 v[82:85], v12
	ds_read_b128 v[86:89], v13
	ds_read_b128 v[94:97], v14
	v_mfma_f32_16x16x32_f16 v[58:61], v[90:93], v[62:65], v[58:61]
	v_mfma_f32_16x16x32_f16 v[50:53], v[98:101], v[62:65], v[50:53]
	v_mfma_f32_16x16x32_f16 v[34:37], v[90:93], v[66:69], v[34:37]
	v_mfma_f32_16x16x32_f16 v[26:29], v[98:101], v[66:69], v[26:29]
	v_mfma_f32_16x16x32_f16 v[38:41], v[90:93], v[70:73], v[38:41]
	v_mfma_f32_16x16x32_f16 v[42:45], v[98:101], v[70:73], v[42:45]
	s_waitcnt lgkmcnt(0)
	v_mfma_f32_16x16x32_f16 v[54:57], v[86:89], v[46:49], v[54:57]
	v_mfma_f32_16x16x32_f16 v[30:33], v[94:97], v[46:49], v[30:33]
	ds_read_b128 v[46:49], v15
	ds_read_b128 v[62:65], v15 offset:2048
	ds_read_b128 v[66:69], v15 offset:4096
	ds_read_b128 v[70:73], v15 offset:6144
	ds_read_b128 v[90:93], v16
	ds_read_b128 v[98:101], v16 offset:2048
	v_mfma_f32_16x16x32_f16 v[58:61], v[86:89], v[74:77], v[58:61]
	v_mfma_f32_16x16x32_f16 v[50:53], v[94:97], v[74:77], v[50:53]
	v_mfma_f32_16x16x32_f16 v[34:37], v[86:89], v[78:81], v[34:37]
	v_mfma_f32_16x16x32_f16 v[26:29], v[94:97], v[78:81], v[26:29]
	v_mfma_f32_16x16x32_f16 v[38:41], v[86:89], v[82:85], v[38:41]
	v_mfma_f32_16x16x32_f16 v[42:45], v[94:97], v[82:85], v[42:45]
	s_add_u32 s6, s2, 0xf00
	s_mov_b32 m0, s22
	s_waitcnt vmcnt(8) lgkmcnt(0)
	s_barrier
	s_addc_u32 s7, s3, 0
	s_add_u32 s14, s4, 0xf00
	global_load_lds_dwordx4 v3, s[6:7]
	s_mov_b32 m0, s19
	s_addc_u32 s15, s5, 0
	global_load_lds_dwordx4 v4, s[6:7]
	s_mov_b32 m0, s20
	s_nop 0
	global_load_lds_dwordx4 v3, s[14:15]
	s_mov_b32 m0, s21
	s_nop 0
	global_load_lds_dwordx4 v4, s[14:15]
	s_waitcnt lgkmcnt(0)
	v_mfma_f32_16x16x32_f16 v[54:57], v[90:93], v[46:49], v[54:57]
	v_mfma_f32_16x16x32_f16 v[30:33], v[98:101], v[46:49], v[30:33]
	ds_read_b128 v[46:49], v17
	ds_read_b128 v[74:77], v18
	ds_read_b128 v[78:81], v19
	ds_read_b128 v[82:85], v20
	ds_read_b128 v[86:89], v21
	ds_read_b128 v[94:97], v22
	v_mfma_f32_16x16x32_f16 v[58:61], v[90:93], v[62:65], v[58:61]
	v_mfma_f32_16x16x32_f16 v[50:53], v[98:101], v[62:65], v[50:53]
	v_mfma_f32_16x16x32_f16 v[34:37], v[90:93], v[66:69], v[34:37]
	v_mfma_f32_16x16x32_f16 v[26:29], v[98:101], v[66:69], v[26:29]
	v_mfma_f32_16x16x32_f16 v[38:41], v[90:93], v[70:73], v[38:41]
	v_mfma_f32_16x16x32_f16 v[42:45], v[98:101], v[70:73], v[42:45]
	s_waitcnt lgkmcnt(0)
	v_mfma_f32_16x16x32_f16 v[54:57], v[86:89], v[46:49], v[54:57]
	v_mfma_f32_16x16x32_f16 v[30:33], v[94:97], v[46:49], v[30:33]
	ds_read_b128 v[46:49], v23
	ds_read_b128 v[62:65], v23 offset:2048
	ds_read_b128 v[66:69], v23 offset:4096
	ds_read_b128 v[70:73], v23 offset:6144
	ds_read_b128 v[90:93], v24
	ds_read_b128 v[98:101], v24 offset:2048
	v_mfma_f32_16x16x32_f16 v[58:61], v[86:89], v[74:77], v[58:61]
	v_mfma_f32_16x16x32_f16 v[50:53], v[94:97], v[74:77], v[50:53]
	v_mfma_f32_16x16x32_f16 v[34:37], v[86:89], v[78:81], v[34:37]
	v_mfma_f32_16x16x32_f16 v[26:29], v[94:97], v[78:81], v[26:29]
	v_mfma_f32_16x16x32_f16 v[38:41], v[86:89], v[82:85], v[38:41]
	v_mfma_f32_16x16x32_f16 v[42:45], v[94:97], v[82:85], v[42:45]
	s_add_u32 s2, s2, 0xf80
	s_mov_b32 m0, s26
	s_waitcnt vmcnt(8) lgkmcnt(0)
	s_barrier
	s_addc_u32 s3, s3, 0
	s_add_u32 s4, s4, 0xf80
	global_load_lds_dwordx4 v3, s[2:3]
	s_mov_b32 m0, s23
	s_addc_u32 s5, s5, 0
	global_load_lds_dwordx4 v4, s[2:3]
	s_mov_b32 m0, s24
	s_nop 0
	global_load_lds_dwordx4 v3, s[4:5]
	s_mov_b32 m0, s25
	s_nop 0
	global_load_lds_dwordx4 v4, s[4:5]
	s_waitcnt lgkmcnt(0)
	v_mfma_f32_16x16x32_f16 v[54:57], v[90:93], v[46:49], v[54:57]
	v_mfma_f32_16x16x32_f16 v[30:33], v[98:101], v[46:49], v[30:33]
	ds_read_b128 v[46:49], v7
	ds_read_b128 v[74:77], v7 offset:2048
	ds_read_b128 v[78:81], v7 offset:4096
	ds_read_b128 v[82:85], v7 offset:6144
	ds_read_b128 v[86:89], v5 offset:16384
	ds_read_b128 v[94:97], v5 offset:18432
	v_mfma_f32_16x16x32_f16 v[58:61], v[90:93], v[62:65], v[58:61]
	v_mfma_f32_16x16x32_f16 v[50:53], v[98:101], v[62:65], v[50:53]
	v_mfma_f32_16x16x32_f16 v[34:37], v[90:93], v[66:69], v[34:37]
	v_mfma_f32_16x16x32_f16 v[26:29], v[98:101], v[66:69], v[26:29]
	v_mfma_f32_16x16x32_f16 v[38:41], v[90:93], v[70:73], v[38:41]
	v_mfma_f32_16x16x32_f16 v[42:45], v[98:101], v[70:73], v[42:45]
	s_waitcnt lgkmcnt(0)
	v_mfma_f32_16x16x32_f16 v[54:57], v[86:89], v[46:49], v[54:57]
	v_mfma_f32_16x16x32_f16 v[30:33], v[94:97], v[46:49], v[30:33]
	ds_read_b128 v[46:49], v6
	ds_read_b128 v[62:65], v6 offset:2048
	ds_read_b128 v[66:69], v6 offset:4096
	ds_read_b128 v[70:73], v6 offset:6144
	ds_read_b128 v[90:93], v8 offset:16384
	ds_read_b128 v[98:101], v8 offset:18432
	v_mfma_f32_16x16x32_f16 v[58:61], v[86:89], v[74:77], v[58:61]
	v_mfma_f32_16x16x32_f16 v[50:53], v[94:97], v[74:77], v[50:53]
	v_mfma_f32_16x16x32_f16 v[34:37], v[86:89], v[78:81], v[34:37]
	v_mfma_f32_16x16x32_f16 v[26:29], v[94:97], v[78:81], v[26:29]
	v_mfma_f32_16x16x32_f16 v[38:41], v[86:89], v[82:85], v[38:41]
	v_mfma_f32_16x16x32_f16 v[42:45], v[94:97], v[82:85], v[42:45]
	s_waitcnt vmcnt(8) lgkmcnt(0)
	s_barrier
	s_waitcnt lgkmcnt(0)
	v_mfma_f32_16x16x32_f16 v[54:57], v[90:93], v[46:49], v[54:57]
	v_mfma_f32_16x16x32_f16 v[30:33], v[98:101], v[46:49], v[30:33]
	ds_read_b128 v[46:49], v7 offset:32768
	ds_read_b128 v[74:77], v7 offset:34816
	ds_read_b128 v[78:81], v7 offset:36864
	ds_read_b128 v[82:85], v7 offset:38912
	ds_read_b128 v[86:89], v5 offset:49152
	ds_read_b128 v[94:97], v5 offset:51200
	v_mfma_f32_16x16x32_f16 v[58:61], v[90:93], v[62:65], v[58:61]
	v_mfma_f32_16x16x32_f16 v[50:53], v[98:101], v[62:65], v[50:53]
	v_mfma_f32_16x16x32_f16 v[34:37], v[90:93], v[66:69], v[34:37]
	v_mfma_f32_16x16x32_f16 v[26:29], v[98:101], v[66:69], v[26:29]
	v_mfma_f32_16x16x32_f16 v[38:41], v[90:93], v[70:73], v[38:41]
	v_mfma_f32_16x16x32_f16 v[42:45], v[98:101], v[70:73], v[42:45]
	s_waitcnt lgkmcnt(0)
	v_mfma_f32_16x16x32_f16 v[54:57], v[86:89], v[46:49], v[54:57]
	v_mfma_f32_16x16x32_f16 v[30:33], v[94:97], v[46:49], v[30:33]
	ds_read_b128 v[46:49], v6 offset:32768
	ds_read_b128 v[62:65], v6 offset:34816
	ds_read_b128 v[66:69], v6 offset:36864
	ds_read_b128 v[4:7], v6 offset:38912
	ds_read_b128 v[70:73], v8 offset:49152
	ds_read_b128 v[90:93], v8 offset:51200
	v_mfma_f32_16x16x32_f16 v[58:61], v[86:89], v[74:77], v[58:61]
	v_mfma_f32_16x16x32_f16 v[50:53], v[94:97], v[74:77], v[50:53]
	v_mfma_f32_16x16x32_f16 v[34:37], v[86:89], v[78:81], v[34:37]
	v_mfma_f32_16x16x32_f16 v[26:29], v[94:97], v[78:81], v[26:29]
	v_mfma_f32_16x16x32_f16 v[38:41], v[86:89], v[82:85], v[38:41]
	v_mfma_f32_16x16x32_f16 v[42:45], v[94:97], v[82:85], v[42:45]
	s_waitcnt vmcnt(0) lgkmcnt(0)
	s_barrier
	s_waitcnt lgkmcnt(0)
	v_mfma_f32_16x16x32_f16 v[54:57], v[70:73], v[46:49], v[54:57]
	v_mfma_f32_16x16x32_f16 v[30:33], v[90:93], v[46:49], v[30:33]
	ds_read_b128 v[46:49], v9
	ds_read_b128 v[74:77], v10
	ds_read_b128 v[8:11], v11
	ds_read_b128 v[78:81], v12
	ds_read_b128 v[82:85], v13
	ds_read_b128 v[86:89], v14
	v_mfma_f32_16x16x32_f16 v[58:61], v[70:73], v[62:65], v[58:61]
	v_mfma_f32_16x16x32_f16 v[50:53], v[90:93], v[62:65], v[50:53]
	v_mfma_f32_16x16x32_f16 v[34:37], v[70:73], v[66:69], v[34:37]
	v_mfma_f32_16x16x32_f16 v[26:29], v[90:93], v[66:69], v[26:29]
	v_mfma_f32_16x16x32_f16 v[38:41], v[70:73], v[4:7], v[38:41]
	v_mfma_f32_16x16x32_f16 v[4:7], v[90:93], v[4:7], v[42:45]
	s_waitcnt lgkmcnt(0)
	v_mfma_f32_16x16x32_f16 v[42:45], v[82:85], v[46:49], v[54:57]
	v_mfma_f32_16x16x32_f16 v[30:33], v[86:89], v[46:49], v[30:33]
	ds_read_b128 v[46:49], v15
	s_nop 0
	ds_read_b128 v[54:57], v15 offset:2048
	ds_read_b128 v[62:65], v15 offset:4096
	ds_read_b128 v[12:15], v15 offset:6144
	ds_read_b128 v[66:69], v16
	ds_read_b128 v[70:73], v16 offset:2048
	v_mfma_f32_16x16x32_f16 v[58:61], v[82:85], v[74:77], v[58:61]
	v_mfma_f32_16x16x32_f16 v[50:53], v[86:89], v[74:77], v[50:53]
	v_mfma_f32_16x16x32_f16 v[34:37], v[82:85], v[8:11], v[34:37]
	v_mfma_f32_16x16x32_f16 v[8:11], v[86:89], v[8:11], v[26:29]
	v_mfma_f32_16x16x32_f16 v[26:29], v[82:85], v[78:81], v[38:41]
	v_mfma_f32_16x16x32_f16 v[4:7], v[86:89], v[78:81], v[4:7]
	s_waitcnt vmcnt(0) lgkmcnt(0)
	s_barrier
	s_waitcnt lgkmcnt(0)
	v_mfma_f32_16x16x32_f16 v[38:41], v[66:69], v[46:49], v[42:45]
	v_mfma_f32_16x16x32_f16 v[30:33], v[70:73], v[46:49], v[30:33]
	s_nop 1
	ds_read_b128 v[42:45], v17
	ds_read_b128 v[46:49], v18
	ds_read_b128 v[16:19], v19
	ds_read_b128 v[74:77], v20
	ds_read_b128 v[78:81], v21
	ds_read_b128 v[82:85], v22
	v_mfma_f32_16x16x32_f16 v[58:61], v[66:69], v[54:57], v[58:61]
	v_mfma_f32_16x16x32_f16 v[50:53], v[70:73], v[54:57], v[50:53]
	v_mfma_f32_16x16x32_f16 v[34:37], v[66:69], v[62:65], v[34:37]
	v_mfma_f32_16x16x32_f16 v[8:11], v[70:73], v[62:65], v[8:11]
	v_mfma_f32_16x16x32_f16 v[26:29], v[66:69], v[12:15], v[26:29]
	v_mfma_f32_16x16x32_f16 v[4:7], v[70:73], v[12:15], v[4:7]
	s_waitcnt lgkmcnt(0)
	v_mfma_f32_16x16x32_f16 v[12:15], v[78:81], v[42:45], v[38:41]
	v_mfma_f32_16x16x32_f16 v[30:33], v[82:85], v[42:45], v[30:33]
	s_nop 1
	ds_read_b128 v[38:41], v23
	ds_read_b128 v[42:45], v23 offset:2048
	ds_read_b128 v[54:57], v23 offset:4096
	ds_read_b128 v[20:23], v23 offset:6144
	ds_read_b128 v[62:65], v24
	ds_read_b128 v[66:69], v24 offset:2048
	v_mfma_f32_16x16x32_f16 v[58:61], v[78:81], v[46:49], v[58:61]
	v_mfma_f32_16x16x32_f16 v[46:49], v[82:85], v[46:49], v[50:53]
	v_mfma_f32_16x16x32_f16 v[34:37], v[78:81], v[16:19], v[34:37]
	v_mfma_f32_16x16x32_f16 v[8:11], v[82:85], v[16:19], v[8:11]
	v_mfma_f32_16x16x32_f16 v[16:19], v[78:81], v[74:77], v[26:29]
	v_mfma_f32_16x16x32_f16 v[4:7], v[82:85], v[74:77], v[4:7]
	s_waitcnt lgkmcnt(0)
	v_mfma_f32_16x16x32_f16 v[12:15], v[62:65], v[38:41], v[12:15]
	v_mfma_f32_16x16x32_f16 v[24:27], v[66:69], v[38:41], v[30:33]
	v_mfma_f32_16x16x32_f16 v[28:31], v[62:65], v[42:45], v[58:61]
	v_mfma_f32_16x16x32_f16 v[38:41], v[66:69], v[42:45], v[46:49]
	v_mfma_f32_16x16x32_f16 v[32:35], v[62:65], v[54:57], v[34:37]
	v_mfma_f32_16x16x32_f16 v[8:11], v[66:69], v[54:57], v[8:11]
	v_mfma_f32_16x16x32_f16 v[16:19], v[62:65], v[20:23], v[16:19]
	v_mfma_f32_16x16x32_f16 v[4:7], v[66:69], v[20:23], v[4:7]
	s_barrier
	v_mul_u32_u24_e32 v46, 0x110, v1
	v_and_b32_e32 v47, 15, v1
	v_lshrrev_b32_e32 v48, 6, v1
	v_lshrrev_b32_e32 v49, 5, v2
	v_lshl_add_u32 v46, v2, 1, v46
	v_lshl_or_b32 v47, v0, 4, v47
	v_lshl_or_b32 v48, v48, 2, v49
	v_lshl_add_u32 v46, v0, 3, v46
	v_lshl_or_b32 v47, v48, 6, v47
	v_cvt_pk_f16_f32 v12, v12, v13
	v_cvt_pk_f16_f32 v13, v14, v15
	ds_write_b64 v46, v[12:13]
	v_cvt_pk_f16_f32 v24, v24, v25
	v_cvt_pk_f16_f32 v25, v26, v27
	ds_write_b64 v46, v[24:25] offset:32
	v_cvt_pk_f16_f32 v28, v28, v29
	v_cvt_pk_f16_f32 v29, v30, v31
	ds_write_b64 v46, v[28:29] offset:4352
	v_cvt_pk_f16_f32 v38, v38, v39
	v_cvt_pk_f16_f32 v39, v40, v41
	ds_write_b64 v46, v[38:39] offset:4384
	v_cvt_pk_f16_f32 v32, v32, v33
	v_cvt_pk_f16_f32 v33, v34, v35
	ds_write_b64 v46, v[32:33] offset:8704
	v_cvt_pk_f16_f32 v8, v8, v9
	v_cvt_pk_f16_f32 v9, v10, v11
	ds_write_b64 v46, v[8:9] offset:8736
	v_cvt_pk_f16_f32 v16, v16, v17
	v_cvt_pk_f16_f32 v17, v18, v19
	ds_write_b64 v46, v[16:17] offset:13056
	v_cvt_pk_f16_f32 v4, v4, v5
	v_cvt_pk_f16_f32 v5, v6, v7
	ds_write_b64 v46, v[4:5] offset:13088
	v_lshrrev_b32_e32 v48, 4, v47
	v_and_b32_e32 v49, 15, v47
	v_mul_u32_u24_e32 v50, 0x110, v48
	v_lshlrev_b32_e32 v48, 11, v48
	v_lshl_add_u32 v50, v49, 4, v50
	v_lshl_add_u32 v48, v49, 4, v48
	s_mul_i32 s4, s8, s12
	s_add_i32 s4, s4, s13
	s_lshl_b32 s5, s11, 1
	s_mul_i32 s2, s4, s9
	s_lshl_b32 s2, s2, 1
	s_add_u32 s2, s2, s5
	s_add_u32 s16, s0, s2
	s_addc_u32 s17, s1, 0
	s_add_u32 s18, s16, 0x10000
	s_addc_u32 s19, s17, 0
	s_add_u32 s20, s18, 0x10000
	s_addc_u32 s21, s19, 0
	s_add_u32 s22, s20, 0x10000
	s_addc_u32 s23, s21, 0
	s_waitcnt lgkmcnt(0)
	s_barrier
	ds_read_b128 v[52:55], v50
	ds_read_b128 v[56:59], v50 offset:8704
	ds_read_b128 v[60:63], v50 offset:17408
	ds_read_b128 v[64:67], v50 offset:26112
	s_waitcnt lgkmcnt(3)
	global_store_dwordx4 v48, v[52:55], s[16:17] sc1
	s_waitcnt lgkmcnt(2)
	global_store_dwordx4 v48, v[56:59], s[18:19] sc1
	s_waitcnt lgkmcnt(1)
	global_store_dwordx4 v48, v[60:63], s[20:21] sc1
	s_waitcnt lgkmcnt(0)
	global_store_dwordx4 v48, v[64:67], s[22:23] sc1
	s_endpgm
	s_endpgm
	s_endpgm
	s_endpgm
	s_endpgm
	s_endpgm
	s_endpgm
	s_endpgm
	s_endpgm
	s_endpgm
	s_endpgm
	s_endpgm
	s_endpgm
	s_endpgm
	s_endpgm
	s_endpgm
	s_endpgm
	s_endpgm
	s_endpgm
	s_endpgm
	s_endpgm
	s_endpgm
	s_endpgm
	s_endpgm
	s_endpgm
	s_endpgm
	s_endpgm
	s_endpgm
	s_endpgm
	s_endpgm
	s_endpgm
	s_endpgm
	s_endpgm
	s_endpgm
	s_endpgm
